# GEMM K-loops: back-to-back s_setprio 0/1 pairs between MFMAs removed
# speedup vs baseline: 1.0056x; 1.0001x over previous
; #define PG8_STAGE(bufoff, gbase, voff) do { const char* sb_ = (gbase); _Pragma("unroll") for (int _i = 0; _i < 2; ++_i) PG8_GLDS(sb_, (voff)[_i], bufoff, _i); } while (0)
; #define PG8_LDA(dst, b, h) do { if constexpr (F8) { _Pragma("unroll") for (int m = 0; m < 4; ++m) dst##8[m] = PG8_RD8(lds + PG8_SA(b, h) + aoff + m * 2048); } else { \
;         _Pragma("unroll") for (int m = 0; m < 4; ++m) _Pragma("unroll") for (int k = 0; k < 2; ++k) dst[m][k] = *(const PG8_LAS bf16x8*)(lds + PG8_SA(b, h) + aoff + m * 2048 + k * 1024); } } while (0)
; #define PG8_LDB(dst, b, h) do { if constexpr (F8) { _Pragma("unroll") for (int n = 0; n < 2; ++n) dst##8[n] = PG8_RD8(lds + PG8_SB(b, h) + boff + n * 2048); } else { \
;         _Pragma("unroll") for (int n = 0; n < 2; ++n) _Pragma("unroll") for (int k = 0; k < 2; ++k) dst[n][k] = *(const PG8_LAS bf16x8*)(lds + PG8_SB(b, h) + boff + n * 2048 + k * 1024); } } while (0)
; #define PG8_WAIT_V(n) asm volatile("s_waitcnt vmcnt(" #n ")" ::: "memory")
;     ...
;         for (int t = 0; t < nt; t += 2) {
;             const bool last = (t == nt - 2);
;             const size_t k1 = (size_t)(t + 1) * kstep;
;             const size_t k2 = last ? 0 : (size_t)(t + 2) * kstep, k3 = k2 + kstep;
;             const char* b2 = last ? nB : cB + (size_t)(t + 2) * kstep; const char* b3 = b2 + kstep;
;             PG8_LDB(B0, 0, 0); PG8_LDB(B1, 0, 1); PG8_SCHED; PG8_LDA(At, 0, 0); PG8_STAGE_A(PG8_SA(1, 1), 1, k1, false);
;             PG8_WAIT_V(8); PG8_WAIT_L(0); PG8_BAR; PG8_MMA(0, 0, At, B0); PG8_MMA(0, 1, At, B1); PG8_BAR; PG8_SCHED;
;             PG8_LDA(At, 0, 1); PG8_STAGE(PG8_SB(0, 0), b2, voffB); PG8_STAGE(PG8_SB(0, 1), b2 + hstep, voffB); PG8_STAGE_A(PG8_SA(0, 0), 0, k2, last);
;             PG8_WAIT_V(8); PG8_WAIT_L(0); PG8_BAR; PG8_MMA(1, 0, At, B0); PG8_MMA(1, 1, At, B1); PG8_BAR; PG8_SCHED;
;             PG8_LDB(B0, 1, 0); PG8_LDB(B1, 1, 1); PG8_SCHED; PG8_LDA(At, 1, 0); PG8_STAGE_A(PG8_SA(0, 1), 1, k2, last);
;             PG8_WAIT_V(8); PG8_WAIT_L(0); PG8_BAR; PG8_MMA(0, 0, At, B0); PG8_MMA(0, 1, At, B1); PG8_BAR; PG8_SCHED;
;             PG8_LDA(At, 1, 1); PG8_STAGE(PG8_SB(1, 0), b3, voffB); PG8_STAGE(PG8_SB(1, 1), b3 + hstep, voffB); PG8_STAGE_A(PG8_SA(1, 0), 0, k3, last);
;             PG8_WAIT_V(8); PG8_WAIT_L(0); PG8_BAR; PG8_MMA(1, 0, At, B0); PG8_MMA(1, 1, At, B1); PG8_BAR; PG8_SCHED;
;         }
.LBB4_306:
	ds_read_b128 v[128:131], v212
	ds_read_b128 v[132:135], v212 offset:16
	ds_read_b128 v[136:139], v212 offset:2048
	ds_read_b128 v[140:143], v212 offset:2064
	ds_read_b128 v[144:147], v213
	ds_read_b128 v[148:151], v213 offset:16
	ds_read_b128 v[152:155], v213 offset:2048
	ds_read_b128 v[156:159], v213 offset:2064
	s_add_i32 s21, s26, 0xfffc0080
	s_add_u32 s28, s8, s26
	s_addc_u32 s29, s9, s27
	s_add_u32 s28, s28, 0xfffc0080
	s_addc_u32 s29, s29, -1
	s_add_u32 s30, s6, s26
	s_addc_u32 s31, s7, s27
	s_cmp_eq_u32 s19, 12
	s_cselect_b32 s21, 0, s21
	s_cselect_b32 s29, s25, s29
	s_cselect_b32 s28, s24, s28
	ds_read_b128 v[160:163], v214
	ds_read_b128 v[164:167], v214 offset:16
	ds_read_b128 v[168:171], v214 offset:2048
	ds_read_b128 v[172:175], v214 offset:2064
	ds_read_b128 v[176:179], v214 offset:4096
	ds_read_b128 v[180:183], v214 offset:4112
	ds_read_b128 v[184:187], v214 offset:6144
	ds_read_b128 v[188:191], v214 offset:6160
	s_mov_b32 m0, s75
	s_nop 0
	global_load_lds_dwordx4 v208, s[30:31]
	s_nop 0
	s_mov_b32 m0, s76
	s_nop 0
	global_load_lds_dwordx4 v210, s[30:31]
	s_waitcnt vmcnt(8)
	s_waitcnt lgkmcnt(0)
	s_barrier
	s_setprio 1
	v_mfma_scale_f32_16x16x128_f8f6f4 v[120:123], v[128:135], v[160:167], v[120:123], v216, v215 op_sel_hi:[0,0,0]
	v_mfma_scale_f32_16x16x128_f8f6f4 v[124:127], v[136:143], v[160:167], v[124:127], v216, v215 op_sel_hi:[0,0,0]
	v_mfma_scale_f32_16x16x128_f8f6f4 v[104:107], v[128:135], v[168:175], v[104:107], v216, v215 op_sel_hi:[0,0,0]
	v_mfma_scale_f32_16x16x128_f8f6f4 v[108:111], v[136:143], v[168:175], v[108:111], v216, v215 op_sel_hi:[0,0,0]
	v_mfma_scale_f32_16x16x128_f8f6f4 v[198:201], v[128:135], v[176:183], v[88:91], v216, v215 op_sel_hi:[0,0,0]
	v_mfma_scale_f32_16x16x128_f8f6f4 v[202:205], v[136:143], v[176:183], v[92:95], v216, v215 op_sel_hi:[0,0,0]
	v_mfma_scale_f32_16x16x128_f8f6f4 v[232:235], v[128:135], v[184:191], v[72:75], v216, v215 op_sel_hi:[0,0,0]
	v_mfma_scale_f32_16x16x128_f8f6f4 v[236:239], v[136:143], v[184:191], v[76:79], v216, v215 op_sel_hi:[0,0,0]
	v_mfma_scale_f32_16x16x128_f8f6f4 v[112:115], v[144:151], v[160:167], v[112:115], v216, v215 op_sel_hi:[0,0,0]
	v_mfma_scale_f32_16x16x128_f8f6f4 v[116:119], v[152:159], v[160:167], v[116:119], v216, v215 op_sel_hi:[0,0,0]
	v_mfma_scale_f32_16x16x128_f8f6f4 v[96:99], v[144:151], v[168:175], v[96:99], v216, v215 op_sel_hi:[0,0,0]
	v_mfma_scale_f32_16x16x128_f8f6f4 v[100:103], v[152:159], v[168:175], v[100:103], v216, v215 op_sel_hi:[0,0,0]
	v_mfma_scale_f32_16x16x128_f8f6f4 v[160:163], v[144:151], v[176:183], v[80:83], v216, v215 op_sel_hi:[0,0,0]
	v_mfma_scale_f32_16x16x128_f8f6f4 v[164:167], v[152:159], v[176:183], v[84:87], v216, v215 op_sel_hi:[0,0,0]
	v_mfma_scale_f32_16x16x128_f8f6f4 v[168:171], v[144:151], v[184:191], v[64:67], v216, v215 op_sel_hi:[0,0,0]
	v_mfma_scale_f32_16x16x128_f8f6f4 v[172:175], v[152:159], v[184:191], v[68:71], v216, v215 op_sel_hi:[0,0,0]
	s_setprio 0
	s_barrier
	s_nop 3
	ds_read_b128 v[64:67], v214 offset:16384
	ds_read_b128 v[68:71], v214 offset:16400
	ds_read_b128 v[72:75], v214 offset:18432
	ds_read_b128 v[76:79], v214 offset:18448
	ds_read_b128 v[80:83], v214 offset:20480
	ds_read_b128 v[84:87], v214 offset:20496
	ds_read_b128 v[88:91], v214 offset:22528
	ds_read_b128 v[92:95], v214 offset:22544
	s_mov_b32 m0, s43
	s_nop 0
	global_load_lds_dwordx4 v209, s[28:29]
	s_cselect_b32 s78, s23, s7
	s_mov_b32 m0, s54
	s_nop 0
	global_load_lds_dwordx4 v211, s[28:29]
	s_cselect_b32 s79, s22, s6
	s_add_u32 s30, s28, 0x40000
	s_addc_u32 s31, s29, 0
	s_mov_b32 m0, s55
	s_nop 0
	global_load_lds_dwordx4 v209, s[30:31]
	s_nop 0
	s_mov_b32 m0, s56
	s_nop 0
	global_load_lds_dwordx4 v211, s[30:31]
	s_add_u32 s30, s79, s21
	s_addc_u32 s31, s78, 0
	s_mov_b32 m0, s42
	s_nop 0
	global_load_lds_dwordx4 v208, s[30:31]
	s_nop 0
	s_mov_b32 m0, s57
	s_nop 0
	global_load_lds_dwordx4 v210, s[30:31]
	s_waitcnt vmcnt(8)
	s_waitcnt lgkmcnt(0)
	s_barrier
	s_setprio 1
	v_mfma_scale_f32_16x16x128_f8f6f4 v[56:59], v[128:135], v[64:71], v[56:59], v216, v215 op_sel_hi:[0,0,0]
	v_mfma_scale_f32_16x16x128_f8f6f4 v[60:63], v[136:143], v[64:71], v[60:63], v216, v215 op_sel_hi:[0,0,0]
	v_mfma_scale_f32_16x16x128_f8f6f4 v[8:11], v[128:135], v[88:95], v[8:11], v216, v215 op_sel_hi:[0,0,0]
	v_mfma_scale_f32_16x16x128_f8f6f4 v[176:179], v[128:135], v[72:79], v[40:43], v216, v215 op_sel_hi:[0,0,0]
	v_mfma_scale_f32_16x16x128_f8f6f4 v[180:183], v[136:143], v[72:79], v[44:47], v216, v215 op_sel_hi:[0,0,0]
	v_mfma_scale_f32_16x16x128_f8f6f4 v[184:187], v[128:135], v[80:87], v[24:27], v216, v215 op_sel_hi:[0,0,0]
	v_mfma_scale_f32_16x16x128_f8f6f4 v[188:191], v[136:143], v[80:87], v[28:31], v216, v215 op_sel_hi:[0,0,0]
	v_mfma_scale_f32_16x16x128_f8f6f4 v[240:243], v[136:143], v[88:95], v[12:15], v216, v215 op_sel_hi:[0,0,0]
	v_mfma_scale_f32_16x16x128_f8f6f4 v[52:55], v[152:159], v[64:71], v[52:55], v216, v215 op_sel_hi:[0,0,0]
	v_mfma_scale_f32_16x16x128_f8f6f4 v[244:247], v[144:151], v[64:71], v[48:51], v216, v215 op_sel_hi:[0,0,0]
	v_mfma_scale_f32_16x16x128_f8f6f4 v[248:251], v[144:151], v[72:79], v[32:35], v216, v215 op_sel_hi:[0,0,0]
	v_mfma_scale_f32_16x16x128_f8f6f4 v[252:255], v[152:159], v[72:79], v[36:39], v216, v215 op_sel_hi:[0,0,0]
	v_mfma_scale_f32_16x16x128_f8f6f4 v[224:227], v[144:151], v[80:87], v[16:19], v216, v215 op_sel_hi:[0,0,0]
	v_mfma_scale_f32_16x16x128_f8f6f4 v[192:195], v[152:159], v[80:87], v[20:23], v216, v215 op_sel_hi:[0,0,0]
	v_mfma_scale_f32_16x16x128_f8f6f4 v[228:231], v[144:151], v[88:95], v[0:3], v216, v215 op_sel_hi:[0,0,0]
	v_mfma_scale_f32_16x16x128_f8f6f4 v[220:223], v[152:159], v[88:95], v[4:7], v216, v215 op_sel_hi:[0,0,0]
	s_setprio 0
	s_barrier
; #define PG8_STAGE(bufoff, gbase, voff) do { const char* sb_ = (gbase); _Pragma("unroll") for (int _i = 0; _i < 2; ++_i) PG8_GLDS(sb_, (voff)[_i], bufoff, _i); } while (0)
; #define PG8_LDA(dst, b, h) do { if constexpr (F8) { _Pragma("unroll") for (int m = 0; m < 4; ++m) dst##8[m] = PG8_RD8(lds + PG8_SA(b, h) + aoff + m * 2048); } else { \
;         _Pragma("unroll") for (int m = 0; m < 4; ++m) _Pragma("unroll") for (int k = 0; k < 2; ++k) dst[m][k] = *(const PG8_LAS bf16x8*)(lds + PG8_SA(b, h) + aoff + m * 2048 + k * 1024); } } while (0)
; #define PG8_LDB(dst, b, h) do { if constexpr (F8) { _Pragma("unroll") for (int n = 0; n < 2; ++n) dst##8[n] = PG8_RD8(lds + PG8_SB(b, h) + boff + n * 2048); } else { \
;         _Pragma("unroll") for (int n = 0; n < 2; ++n) _Pragma("unroll") for (int k = 0; k < 2; ++k) dst[n][k] = *(const PG8_LAS bf16x8*)(lds + PG8_SB(b, h) + boff + n * 2048 + k * 1024); } } while (0)
; #define PG8_WAIT_V(n) asm volatile("s_waitcnt vmcnt(" #n ")" ::: "memory")
;     ...
;         for (int t = 0; t < nt; t += 2) {
;             const bool last = (t == nt - 2);
;             const size_t k1 = (size_t)(t + 1) * kstep;
;             const size_t k2 = last ? 0 : (size_t)(t + 2) * kstep, k3 = k2 + kstep;
;             const char* b2 = last ? nB : cB + (size_t)(t + 2) * kstep; const char* b3 = b2 + kstep;
;             PG8_LDB(B0, 0, 0); PG8_LDB(B1, 0, 1); PG8_SCHED; PG8_LDA(At, 0, 0); PG8_STAGE_A(PG8_SA(1, 1), 1, k1, false);
;             PG8_WAIT_V(8); PG8_WAIT_L(0); PG8_BAR; PG8_MMA(0, 0, At, B0); PG8_MMA(0, 1, At, B1); PG8_BAR; PG8_SCHED;
;             PG8_LDA(At, 0, 1); PG8_STAGE(PG8_SB(0, 0), b2, voffB); PG8_STAGE(PG8_SB(0, 1), b2 + hstep, voffB); PG8_STAGE_A(PG8_SA(0, 0), 0, k2, last);
;             PG8_WAIT_V(8); PG8_WAIT_L(0); PG8_BAR; PG8_MMA(1, 0, At, B0); PG8_MMA(1, 1, At, B1); PG8_BAR; PG8_SCHED;
;             PG8_LDB(B0, 1, 0); PG8_LDB(B1, 1, 1); PG8_SCHED; PG8_LDA(At, 1, 0); PG8_STAGE_A(PG8_SA(0, 1), 1, k2, last);
;             PG8_WAIT_V(8); PG8_WAIT_L(0); PG8_BAR; PG8_MMA(0, 0, At, B0); PG8_MMA(0, 1, At, B1); PG8_BAR; PG8_SCHED;
;             PG8_LDA(At, 1, 1); PG8_STAGE(PG8_SB(1, 0), b3, voffB); PG8_STAGE(PG8_SB(1, 1), b3 + hstep, voffB); PG8_STAGE_A(PG8_SA(1, 0), 0, k3, last);
;             PG8_WAIT_V(8); PG8_WAIT_L(0); PG8_BAR; PG8_MMA(1, 0, At, B0); PG8_MMA(1, 1, At, B1); PG8_BAR; PG8_SCHED;
;         }
	s_nop 3
	ds_read_b128 v[0:3], v217
	ds_read_b128 v[4:7], v217 offset:16
	ds_read_b128 v[12:15], v217 offset:2048
	ds_read_b128 v[16:19], v217 offset:2064
	ds_read_b128 v[128:131], v218
	ds_read_b128 v[132:135], v218 offset:16
	ds_read_b128 v[136:139], v218 offset:2048
	ds_read_b128 v[140:143], v218 offset:2064
	ds_read_b128 v[20:23], v214 offset:32768
	ds_read_b128 v[24:27], v214 offset:32784
	ds_read_b128 v[28:31], v214 offset:34816
	ds_read_b128 v[32:35], v214 offset:34832
	ds_read_b128 v[36:39], v214 offset:36864
	ds_read_b128 v[40:43], v214 offset:36880
	ds_read_b128 v[44:47], v214 offset:38912
	ds_read_b128 v[48:51], v214 offset:38928
	s_add_u32 s78, s30, 0x40000
	s_addc_u32 s79, s31, 0
	s_mov_b32 m0, s58
	s_nop 0
	global_load_lds_dwordx4 v208, s[78:79]
	s_nop 0
	s_mov_b32 m0, s59
	s_nop 0
	global_load_lds_dwordx4 v210, s[78:79]
	s_waitcnt vmcnt(8)
	s_waitcnt lgkmcnt(0)
	s_barrier
	s_setprio 1
	v_mfma_scale_f32_16x16x128_f8f6f4 v[120:123], v[0:7], v[20:27], v[120:123], v216, v215 op_sel_hi:[0,0,0]
	v_mfma_scale_f32_16x16x128_f8f6f4 v[124:127], v[12:19], v[20:27], v[124:127], v216, v215 op_sel_hi:[0,0,0]
	v_mfma_scale_f32_16x16x128_f8f6f4 v[104:107], v[0:7], v[28:35], v[104:107], v216, v215 op_sel_hi:[0,0,0]
	v_mfma_scale_f32_16x16x128_f8f6f4 v[108:111], v[12:19], v[28:35], v[108:111], v216, v215 op_sel_hi:[0,0,0]
	v_mfma_scale_f32_16x16x128_f8f6f4 v[88:91], v[0:7], v[36:43], v[198:201], v216, v215 op_sel_hi:[0,0,0]
	v_mfma_scale_f32_16x16x128_f8f6f4 v[92:95], v[12:19], v[36:43], v[202:205], v216, v215 op_sel_hi:[0,0,0]
	v_mfma_scale_f32_16x16x128_f8f6f4 v[72:75], v[0:7], v[44:51], v[232:235], v216, v215 op_sel_hi:[0,0,0]
	v_mfma_scale_f32_16x16x128_f8f6f4 v[76:79], v[12:19], v[44:51], v[236:239], v216, v215 op_sel_hi:[0,0,0]
	v_mfma_scale_f32_16x16x128_f8f6f4 v[112:115], v[128:135], v[20:27], v[112:115], v216, v215 op_sel_hi:[0,0,0]
	v_mfma_scale_f32_16x16x128_f8f6f4 v[116:119], v[136:143], v[20:27], v[116:119], v216, v215 op_sel_hi:[0,0,0]
	v_mfma_scale_f32_16x16x128_f8f6f4 v[96:99], v[128:135], v[28:35], v[96:99], v216, v215 op_sel_hi:[0,0,0]
	v_mfma_scale_f32_16x16x128_f8f6f4 v[100:103], v[136:143], v[28:35], v[100:103], v216, v215 op_sel_hi:[0,0,0]
	v_mfma_scale_f32_16x16x128_f8f6f4 v[80:83], v[128:135], v[36:43], v[160:163], v216, v215 op_sel_hi:[0,0,0]
	v_mfma_scale_f32_16x16x128_f8f6f4 v[84:87], v[136:143], v[36:43], v[164:167], v216, v215 op_sel_hi:[0,0,0]
	v_mfma_scale_f32_16x16x128_f8f6f4 v[64:67], v[128:135], v[44:51], v[168:171], v216, v215 op_sel_hi:[0,0,0]
	v_mfma_scale_f32_16x16x128_f8f6f4 v[68:71], v[136:143], v[44:51], v[172:175], v216, v215 op_sel_hi:[0,0,0]
	s_setprio 0
	s_barrier
	ds_read_b128 v[32:35], v214 offset:49152
	ds_read_b128 v[36:39], v214 offset:49168
	ds_read_b128 v[144:147], v214 offset:51200
	ds_read_b128 v[148:151], v214 offset:51216
	ds_read_b128 v[152:155], v214 offset:53248
	ds_read_b128 v[156:159], v214 offset:53264
	ds_read_b128 v[160:163], v214 offset:55296
	ds_read_b128 v[164:167], v214 offset:55312
	s_add_u32 s78, s28, 0x80
	s_addc_u32 s79, s29, 0
	s_mov_b32 m0, s63
	s_nop 0
	global_load_lds_dwordx4 v209, s[78:79]
	s_add_u32 s28, s28, 0x40080
	s_mov_b32 m0, s64
	s_nop 0
	global_load_lds_dwordx4 v211, s[78:79]
	s_addc_u32 s29, s29, 0
	s_mov_b32 m0, s67
	s_nop 0
	global_load_lds_dwordx4 v209, s[28:29]
	s_nop 0
	s_mov_b32 m0, s74
	s_nop 0
	global_load_lds_dwordx4 v211, s[28:29]
	s_add_u32 s28, s30, 0x80
	s_addc_u32 s29, s31, 0
	s_mov_b32 m0, s65
	s_nop 0
	global_load_lds_dwordx4 v208, s[28:29]
	s_nop 0
	s_mov_b32 m0, s66
	s_nop 0
	global_load_lds_dwordx4 v210, s[28:29]
	s_waitcnt vmcnt(8)
	s_waitcnt lgkmcnt(0)
	s_barrier
	s_setprio 1
	v_mfma_scale_f32_16x16x128_f8f6f4 v[56:59], v[0:7], v[32:39], v[56:59], v216, v215 op_sel_hi:[0,0,0]
	v_mfma_scale_f32_16x16x128_f8f6f4 v[60:63], v[12:19], v[32:39], v[60:63], v216, v215 op_sel_hi:[0,0,0]
	v_mfma_scale_f32_16x16x128_f8f6f4 v[40:43], v[0:7], v[144:151], v[176:179], v216, v215 op_sel_hi:[0,0,0]
	v_mfma_scale_f32_16x16x128_f8f6f4 v[44:47], v[12:19], v[144:151], v[180:183], v216, v215 op_sel_hi:[0,0,0]
	v_mfma_scale_f32_16x16x128_f8f6f4 v[24:27], v[0:7], v[152:159], v[184:187], v216, v215 op_sel_hi:[0,0,0]
	v_mfma_scale_f32_16x16x128_f8f6f4 v[28:31], v[12:19], v[152:159], v[188:191], v216, v215 op_sel_hi:[0,0,0]
	v_mfma_scale_f32_16x16x128_f8f6f4 v[8:11], v[0:7], v[160:167], v[8:11], v216, v215 op_sel_hi:[0,0,0]
	v_mfma_scale_f32_16x16x128_f8f6f4 v[12:15], v[12:19], v[160:167], v[240:243], v216, v215 op_sel_hi:[0,0,0]
	v_mfma_scale_f32_16x16x128_f8f6f4 v[48:51], v[128:135], v[32:39], v[244:247], v216, v215 op_sel_hi:[0,0,0]
	v_mfma_scale_f32_16x16x128_f8f6f4 v[52:55], v[136:143], v[32:39], v[52:55], v216, v215 op_sel_hi:[0,0,0]
	v_mfma_scale_f32_16x16x128_f8f6f4 v[32:35], v[128:135], v[144:151], v[248:251], v216, v215 op_sel_hi:[0,0,0]
	v_mfma_scale_f32_16x16x128_f8f6f4 v[36:39], v[136:143], v[144:151], v[252:255], v216, v215 op_sel_hi:[0,0,0]
	v_mfma_scale_f32_16x16x128_f8f6f4 v[16:19], v[128:135], v[152:159], v[224:227], v216, v215 op_sel_hi:[0,0,0]
	v_mfma_scale_f32_16x16x128_f8f6f4 v[20:23], v[136:143], v[152:159], v[192:195], v216, v215 op_sel_hi:[0,0,0]
	v_mfma_scale_f32_16x16x128_f8f6f4 v[0:3], v[128:135], v[160:167], v[228:231], v216, v215 op_sel_hi:[0,0,0]
	v_mfma_scale_f32_16x16x128_f8f6f4 v[4:7], v[136:143], v[160:167], v[220:223], v216, v215 op_sel_hi:[0,0,0]
	s_setprio 0
	s_barrier
	s_add_i32 s19, s19, 2
	s_add_u32 s26, s26, 0x100
	s_addc_u32 s27, s27, 0
	s_cmp_gt_u32 s19, 13
	s_cbranch_scc0 .LBB4_306
	s_and_b64 vcc, exec, s[16:17]
	s_cbranch_vccz .LBB4_309
	s_barrier

; #define PG8_STAGE(bufoff, gbase, voff) do { const char* sb_ = (gbase); _Pragma("unroll") for (int _i = 0; _i < 2; ++_i) PG8_GLDS(sb_, (voff)[_i], bufoff, _i); } while (0)
; #define PG8_LDA(dst, b, h) do { if constexpr (F8) { _Pragma("unroll") for (int m = 0; m < 4; ++m) dst##8[m] = PG8_RD8(lds + PG8_SA(b, h) + aoff + m * 2048); } else { \
;         _Pragma("unroll") for (int m = 0; m < 4; ++m) _Pragma("unroll") for (int k = 0; k < 2; ++k) dst[m][k] = *(const PG8_LAS bf16x8*)(lds + PG8_SA(b, h) + aoff + m * 2048 + k * 1024); } } while (0)
; #define PG8_LDB(dst, b, h) do { if constexpr (F8) { _Pragma("unroll") for (int n = 0; n < 2; ++n) dst##8[n] = PG8_RD8(lds + PG8_SB(b, h) + boff + n * 2048); } else { \
;         _Pragma("unroll") for (int n = 0; n < 2; ++n) _Pragma("unroll") for (int k = 0; k < 2; ++k) dst[n][k] = *(const PG8_LAS bf16x8*)(lds + PG8_SB(b, h) + boff + n * 2048 + k * 1024); } } while (0)
; #define PG8_WAIT_V(n) asm volatile("s_waitcnt vmcnt(" #n ")" ::: "memory")
;     ...
;         for (int t = 0; t < nt; t += 2) {
;             const bool last = (t == nt - 2);
;             const size_t k1 = (size_t)(t + 1) * kstep;
;             const size_t k2 = last ? 0 : (size_t)(t + 2) * kstep, k3 = k2 + kstep;
;             const char* b2 = last ? nB : cB + (size_t)(t + 2) * kstep; const char* b3 = b2 + kstep;
;             PG8_LDB(B0, 0, 0); PG8_LDB(B1, 0, 1); PG8_SCHED; PG8_LDA(At, 0, 0); PG8_STAGE_A(PG8_SA(1, 1), 1, k1, false);
;             PG8_WAIT_V(8); PG8_WAIT_L(0); PG8_BAR; PG8_MMA(0, 0, At, B0); PG8_MMA(0, 1, At, B1); PG8_BAR; PG8_SCHED;
;             PG8_LDA(At, 0, 1); PG8_STAGE(PG8_SB(0, 0), b2, voffB); PG8_STAGE(PG8_SB(0, 1), b2 + hstep, voffB); PG8_STAGE_A(PG8_SA(0, 0), 0, k2, last);
;             PG8_WAIT_V(8); PG8_WAIT_L(0); PG8_BAR; PG8_MMA(1, 0, At, B0); PG8_MMA(1, 1, At, B1); PG8_BAR; PG8_SCHED;
;             PG8_LDB(B0, 1, 0); PG8_LDB(B1, 1, 1); PG8_SCHED; PG8_LDA(At, 1, 0); PG8_STAGE_A(PG8_SA(0, 1), 1, k2, last);
;             PG8_WAIT_V(8); PG8_WAIT_L(0); PG8_BAR; PG8_MMA(0, 0, At, B0); PG8_MMA(0, 1, At, B1); PG8_BAR; PG8_SCHED;
;             PG8_LDA(At, 1, 1); PG8_STAGE(PG8_SB(1, 0), b3, voffB); PG8_STAGE(PG8_SB(1, 1), b3 + hstep, voffB); PG8_STAGE_A(PG8_SA(1, 0), 0, k3, last);
;             PG8_WAIT_V(8); PG8_WAIT_L(0); PG8_BAR; PG8_MMA(1, 0, At, B0); PG8_MMA(1, 1, At, B1); PG8_BAR; PG8_SCHED;
;         }
.LBB4_1055:
	ds_read_b128 v[152:155], v149
	ds_read_b128 v[156:159], v149 offset:1024
	ds_read_b128 v[160:163], v149 offset:2048
	ds_read_b128 v[164:167], v149 offset:3072
	ds_read_b128 v[168:171], v150
	ds_read_b128 v[172:175], v150 offset:1024
	ds_read_b128 v[176:179], v150 offset:2048
	ds_read_b128 v[180:183], v150 offset:3072
	s_add_u32 s36, s34, 0x100
	s_addc_u32 s37, s35, 0
	s_add_u32 s80, s77, s34
	s_addc_u32 s81, s78, s35
	s_cmp_eq_u32 s79, 28
	s_cselect_b64 s[40:41], -1, 0
	s_and_b64 s[38:39], s[40:41], exec
	s_cselect_b32 s82, 0, s36
	s_cselect_b32 s39, s21, s81
	s_cselect_b32 s38, s23, s80
	v_lshl_add_u64 v[216:217], v[144:145], 0, s[34:35]
	s_add_i32 m0, s29, 0xc000
	ds_read_b128 v[184:187], v151
	ds_read_b128 v[188:191], v151 offset:1024
	ds_read_b128 v[192:195], v151 offset:2048
	ds_read_b128 v[196:199], v151 offset:3072
	ds_read_b128 v[200:203], v151 offset:4096
	ds_read_b128 v[204:207], v151 offset:5120
	ds_read_b128 v[208:211], v151 offset:6144
	ds_read_b128 v[212:215], v151 offset:7168
	global_load_lds_dwordx4 v[216:217], off
	v_lshl_add_u64 v[216:217], v[146:147], 0, s[34:35]
	s_add_i32 m0, s29, 0xe000
	s_nop 0
	global_load_lds_dwordx4 v[216:217], off
	s_waitcnt vmcnt(8)
	s_waitcnt lgkmcnt(0)
	s_barrier
	s_setprio 1
	v_mfma_f32_16x16x32_bf16 v[124:127], v[152:155], v[184:187], v[124:127]
	v_mfma_f32_16x16x32_bf16 v[120:123], v[160:163], v[184:187], v[120:123]
	v_mfma_f32_16x16x32_bf16 v[112:115], v[152:155], v[192:195], v[112:115]
	v_mfma_f32_16x16x32_bf16 v[104:107], v[160:163], v[192:195], v[104:107]
	v_mfma_f32_16x16x32_bf16 v[96:99], v[152:155], v[200:203], v[96:99]
	v_mfma_f32_16x16x32_bf16 v[88:91], v[160:163], v[200:203], v[88:91]
	v_mfma_f32_16x16x32_bf16 v[80:83], v[152:155], v[208:211], v[80:83]
	v_mfma_f32_16x16x32_bf16 v[72:75], v[160:163], v[208:211], v[72:75]
	v_mfma_f32_16x16x32_bf16 v[124:127], v[156:159], v[188:191], v[124:127]
	v_mfma_f32_16x16x32_bf16 v[120:123], v[164:167], v[188:191], v[120:123]
	v_mfma_f32_16x16x32_bf16 v[112:115], v[156:159], v[196:199], v[112:115]
	v_mfma_f32_16x16x32_bf16 v[104:107], v[164:167], v[196:199], v[104:107]
	v_mfma_f32_16x16x32_bf16 v[96:99], v[156:159], v[204:207], v[96:99]
	v_mfma_f32_16x16x32_bf16 v[88:91], v[164:167], v[204:207], v[88:91]
	v_mfma_f32_16x16x32_bf16 v[80:83], v[156:159], v[212:215], v[80:83]
	v_mfma_f32_16x16x32_bf16 v[72:75], v[164:167], v[212:215], v[72:75]
	v_mfma_f32_16x16x32_bf16 v[116:119], v[168:171], v[184:187], v[116:119]
	v_mfma_f32_16x16x32_bf16 v[108:111], v[176:179], v[184:187], v[108:111]
	v_mfma_f32_16x16x32_bf16 v[100:103], v[168:171], v[192:195], v[100:103]
	v_mfma_f32_16x16x32_bf16 v[92:95], v[176:179], v[192:195], v[92:95]
	v_mfma_f32_16x16x32_bf16 v[84:87], v[168:171], v[200:203], v[84:87]
	v_mfma_f32_16x16x32_bf16 v[76:79], v[176:179], v[200:203], v[76:79]
	v_mfma_f32_16x16x32_bf16 v[68:71], v[168:171], v[208:211], v[68:71]
	v_mfma_f32_16x16x32_bf16 v[64:67], v[176:179], v[208:211], v[64:67]
	v_mfma_f32_16x16x32_bf16 v[116:119], v[172:175], v[188:191], v[116:119]
	v_mfma_f32_16x16x32_bf16 v[108:111], v[180:183], v[188:191], v[108:111]
	v_mfma_f32_16x16x32_bf16 v[100:103], v[172:175], v[196:199], v[100:103]
	v_mfma_f32_16x16x32_bf16 v[92:95], v[180:183], v[196:199], v[92:95]
	v_mfma_f32_16x16x32_bf16 v[84:87], v[172:175], v[204:207], v[84:87]
	v_mfma_f32_16x16x32_bf16 v[76:79], v[180:183], v[204:207], v[76:79]
	v_mfma_f32_16x16x32_bf16 v[68:71], v[172:175], v[212:215], v[68:71]
	v_mfma_f32_16x16x32_bf16 v[64:67], v[180:183], v[212:215], v[64:67]
	s_setprio 0
	s_barrier
	s_add_i32 s34, s67, s57
	v_lshl_add_u64 v[216:217], s[38:39], 0, v[130:131]
	s_mov_b32 m0, s34
	ds_read_b128 v[184:187], v151 offset:16384
	ds_read_b128 v[188:191], v151 offset:17408
	ds_read_b128 v[192:195], v151 offset:18432
	ds_read_b128 v[196:199], v151 offset:19456
	ds_read_b128 v[200:203], v151 offset:20480
	ds_read_b128 v[204:207], v151 offset:21504
	ds_read_b128 v[208:211], v151 offset:22528
	ds_read_b128 v[212:215], v151 offset:23552
	global_load_lds_dwordx4 v[216:217], off
	s_add_i32 m0, s34, 0x2000
	s_add_u32 s34, s38, 0x80000
	v_lshl_add_u64 v[218:219], s[38:39], 0, v[134:135]
	s_addc_u32 s35, s39, 0
	s_add_i32 s80, s74, s57
	global_load_lds_dwordx4 v[218:219], off
	v_lshl_add_u64 v[220:221], s[34:35], 0, v[130:131]
	s_mov_b32 m0, s80
	s_nop 0
	global_load_lds_dwordx4 v[220:221], off
	v_lshl_add_u64 v[220:221], s[34:35], 0, v[134:135]
	s_add_i32 m0, s80, 0x2000
	s_and_b64 s[34:35], s[2:3], s[40:41]
	s_and_b64 s[34:35], s[34:35], exec
	s_cselect_b32 s34, s24, s30
	s_cselect_b32 s35, s25, s31
	s_add_u32 s34, s34, s82
	s_addc_u32 s35, s35, 0
	global_load_lds_dwordx4 v[220:221], off
	v_lshl_add_u64 v[220:221], s[34:35], 0, v[128:129]
	s_mov_b32 m0, s29
	v_lshl_add_u64 v[222:223], s[34:35], 0, v[132:133]
	global_load_lds_dwordx4 v[220:221], off
	s_mov_b32 m0, s58
	s_nop 0
	global_load_lds_dwordx4 v[222:223], off
	s_waitcnt vmcnt(8)
	s_waitcnt lgkmcnt(0)
	s_barrier
; #define PG8_STAGE(bufoff, gbase, voff) do { const char* sb_ = (gbase); _Pragma("unroll") for (int _i = 0; _i < 2; ++_i) PG8_GLDS(sb_, (voff)[_i], bufoff, _i); } while (0)
; #define PG8_LDA(dst, b, h) do { if constexpr (F8) { _Pragma("unroll") for (int m = 0; m < 4; ++m) dst##8[m] = PG8_RD8(lds + PG8_SA(b, h) + aoff + m * 2048); } else { \
;         _Pragma("unroll") for (int m = 0; m < 4; ++m) _Pragma("unroll") for (int k = 0; k < 2; ++k) dst[m][k] = *(const PG8_LAS bf16x8*)(lds + PG8_SA(b, h) + aoff + m * 2048 + k * 1024); } } while (0)
; #define PG8_LDB(dst, b, h) do { if constexpr (F8) { _Pragma("unroll") for (int n = 0; n < 2; ++n) dst##8[n] = PG8_RD8(lds + PG8_SB(b, h) + boff + n * 2048); } else { \
;         _Pragma("unroll") for (int n = 0; n < 2; ++n) _Pragma("unroll") for (int k = 0; k < 2; ++k) dst[n][k] = *(const PG8_LAS bf16x8*)(lds + PG8_SB(b, h) + boff + n * 2048 + k * 1024); } } while (0)
; #define PG8_WAIT_V(n) asm volatile("s_waitcnt vmcnt(" #n ")" ::: "memory")
;     ...
;         for (int t = 0; t < nt; t += 2) {
;             const bool last = (t == nt - 2);
;             const size_t k1 = (size_t)(t + 1) * kstep;
;             const size_t k2 = last ? 0 : (size_t)(t + 2) * kstep, k3 = k2 + kstep;
;             const char* b2 = last ? nB : cB + (size_t)(t + 2) * kstep; const char* b3 = b2 + kstep;
;             PG8_LDB(B0, 0, 0); PG8_LDB(B1, 0, 1); PG8_SCHED; PG8_LDA(At, 0, 0); PG8_STAGE_A(PG8_SA(1, 1), 1, k1, false);
;             PG8_WAIT_V(8); PG8_WAIT_L(0); PG8_BAR; PG8_MMA(0, 0, At, B0); PG8_MMA(0, 1, At, B1); PG8_BAR; PG8_SCHED;
;             PG8_LDA(At, 0, 1); PG8_STAGE(PG8_SB(0, 0), b2, voffB); PG8_STAGE(PG8_SB(0, 1), b2 + hstep, voffB); PG8_STAGE_A(PG8_SA(0, 0), 0, k2, last);
;             PG8_WAIT_V(8); PG8_WAIT_L(0); PG8_BAR; PG8_MMA(1, 0, At, B0); PG8_MMA(1, 1, At, B1); PG8_BAR; PG8_SCHED;
;             PG8_LDB(B0, 1, 0); PG8_LDB(B1, 1, 1); PG8_SCHED; PG8_LDA(At, 1, 0); PG8_STAGE_A(PG8_SA(0, 1), 1, k2, last);
;             PG8_WAIT_V(8); PG8_WAIT_L(0); PG8_BAR; PG8_MMA(0, 0, At, B0); PG8_MMA(0, 1, At, B1); PG8_BAR; PG8_SCHED;
;             PG8_LDA(At, 1, 1); PG8_STAGE(PG8_SB(1, 0), b3, voffB); PG8_STAGE(PG8_SB(1, 1), b3 + hstep, voffB); PG8_STAGE_A(PG8_SA(1, 0), 0, k3, last);
;             PG8_WAIT_V(8); PG8_WAIT_L(0); PG8_BAR; PG8_MMA(1, 0, At, B0); PG8_MMA(1, 1, At, B1); PG8_BAR; PG8_SCHED;
;         }
	s_setprio 1
	v_mfma_f32_16x16x32_bf16 v[60:63], v[152:155], v[184:187], v[60:63]
	v_mfma_f32_16x16x32_bf16 v[56:59], v[160:163], v[184:187], v[56:59]
	v_mfma_f32_16x16x32_bf16 v[52:55], v[152:155], v[192:195], v[52:55]
	v_mfma_f32_16x16x32_bf16 v[44:47], v[160:163], v[192:195], v[44:47]
	v_mfma_f32_16x16x32_bf16 v[36:39], v[152:155], v[200:203], v[36:39]
	v_mfma_f32_16x16x32_bf16 v[28:31], v[160:163], v[200:203], v[28:31]
	v_mfma_f32_16x16x32_bf16 v[20:23], v[152:155], v[208:211], v[20:23]
	v_mfma_f32_16x16x32_bf16 v[12:15], v[160:163], v[208:211], v[12:15]
	v_mfma_f32_16x16x32_bf16 v[60:63], v[156:159], v[188:191], v[60:63]
	v_mfma_f32_16x16x32_bf16 v[56:59], v[164:167], v[188:191], v[56:59]
	v_mfma_f32_16x16x32_bf16 v[52:55], v[156:159], v[196:199], v[52:55]
	v_mfma_f32_16x16x32_bf16 v[44:47], v[164:167], v[196:199], v[44:47]
	v_mfma_f32_16x16x32_bf16 v[36:39], v[156:159], v[204:207], v[36:39]
	v_mfma_f32_16x16x32_bf16 v[28:31], v[164:167], v[204:207], v[28:31]
	v_mfma_f32_16x16x32_bf16 v[20:23], v[156:159], v[212:215], v[20:23]
	v_mfma_f32_16x16x32_bf16 v[12:15], v[164:167], v[212:215], v[12:15]
	v_mfma_f32_16x16x32_bf16 v[48:51], v[168:171], v[184:187], v[48:51]
	v_mfma_f32_16x16x32_bf16 v[40:43], v[176:179], v[184:187], v[40:43]
	v_mfma_f32_16x16x32_bf16 v[32:35], v[168:171], v[192:195], v[32:35]
	v_mfma_f32_16x16x32_bf16 v[24:27], v[176:179], v[192:195], v[24:27]
	v_mfma_f32_16x16x32_bf16 v[16:19], v[168:171], v[200:203], v[16:19]
	v_mfma_f32_16x16x32_bf16 v[8:11], v[176:179], v[200:203], v[8:11]
	v_mfma_f32_16x16x32_bf16 v[4:7], v[168:171], v[208:211], v[4:7]
	v_mfma_f32_16x16x32_bf16 v[0:3], v[176:179], v[208:211], v[0:3]
	v_mfma_f32_16x16x32_bf16 v[48:51], v[172:175], v[188:191], v[48:51]
	v_mfma_f32_16x16x32_bf16 v[40:43], v[180:183], v[188:191], v[40:43]
	v_mfma_f32_16x16x32_bf16 v[32:35], v[172:175], v[196:199], v[32:35]
	v_mfma_f32_16x16x32_bf16 v[24:27], v[180:183], v[196:199], v[24:27]
	v_mfma_f32_16x16x32_bf16 v[16:19], v[172:175], v[204:207], v[16:19]
	v_mfma_f32_16x16x32_bf16 v[8:11], v[180:183], v[204:207], v[8:11]
	v_mfma_f32_16x16x32_bf16 v[4:7], v[172:175], v[212:215], v[4:7]
	v_mfma_f32_16x16x32_bf16 v[0:3], v[180:183], v[212:215], v[0:3]
	s_setprio 0
	s_barrier
	s_add_i32 s40, 0, 0x18000
	s_add_i32 s41, 0, 0x1c000
	v_add_u32_e32 v164, s40, v148
	v_add_u32_e32 v180, s41, v148
	ds_read_b128 v[152:155], v164
	ds_read_b128 v[156:159], v164 offset:1024
	ds_read_b128 v[160:163], v164 offset:2048
	ds_read_b128 v[164:167], v164 offset:3072
	ds_read_b128 v[168:171], v180
	ds_read_b128 v[172:175], v180 offset:1024
	ds_read_b128 v[176:179], v180 offset:2048
	ds_read_b128 v[180:183], v180 offset:3072
	s_add_u32 s34, s34, 0x80000
	s_addc_u32 s35, s35, 0
	s_mov_b32 m0, s59
	v_lshl_add_u64 v[224:225], s[34:35], 0, v[128:129]
	ds_read_b128 v[184:187], v151 offset:32768
	ds_read_b128 v[188:191], v151 offset:33792
	ds_read_b128 v[192:195], v151 offset:34816
	ds_read_b128 v[196:199], v151 offset:35840
	ds_read_b128 v[200:203], v151 offset:36864
	ds_read_b128 v[204:207], v151 offset:37888
	ds_read_b128 v[208:211], v151 offset:38912
	ds_read_b128 v[212:215], v151 offset:39936
	global_load_lds_dwordx4 v[224:225], off
	v_lshl_add_u64 v[224:225], s[34:35], 0, v[132:133]
	s_mov_b32 m0, s60
	s_nop 0
	global_load_lds_dwordx4 v[224:225], off
	s_waitcnt vmcnt(8)
	s_waitcnt lgkmcnt(0)
	s_barrier
	s_setprio 1
	v_mfma_f32_16x16x32_bf16 v[124:127], v[152:155], v[184:187], v[124:127]
	v_mfma_f32_16x16x32_bf16 v[120:123], v[160:163], v[184:187], v[120:123]
	v_mfma_f32_16x16x32_bf16 v[112:115], v[152:155], v[192:195], v[112:115]
	v_mfma_f32_16x16x32_bf16 v[104:107], v[160:163], v[192:195], v[104:107]
	v_mfma_f32_16x16x32_bf16 v[96:99], v[152:155], v[200:203], v[96:99]
	v_mfma_f32_16x16x32_bf16 v[88:91], v[160:163], v[200:203], v[88:91]
	v_mfma_f32_16x16x32_bf16 v[80:83], v[152:155], v[208:211], v[80:83]
	v_mfma_f32_16x16x32_bf16 v[72:75], v[160:163], v[208:211], v[72:75]
	v_mfma_f32_16x16x32_bf16 v[124:127], v[156:159], v[188:191], v[124:127]
	v_mfma_f32_16x16x32_bf16 v[120:123], v[164:167], v[188:191], v[120:123]
	v_mfma_f32_16x16x32_bf16 v[112:115], v[156:159], v[196:199], v[112:115]
	v_mfma_f32_16x16x32_bf16 v[104:107], v[164:167], v[196:199], v[104:107]
	v_mfma_f32_16x16x32_bf16 v[96:99], v[156:159], v[204:207], v[96:99]
	v_mfma_f32_16x16x32_bf16 v[88:91], v[164:167], v[204:207], v[88:91]
	v_mfma_f32_16x16x32_bf16 v[80:83], v[156:159], v[212:215], v[80:83]
	v_mfma_f32_16x16x32_bf16 v[72:75], v[164:167], v[212:215], v[72:75]
	v_mfma_f32_16x16x32_bf16 v[116:119], v[168:171], v[184:187], v[116:119]
	v_mfma_f32_16x16x32_bf16 v[108:111], v[176:179], v[184:187], v[108:111]
	v_mfma_f32_16x16x32_bf16 v[100:103], v[168:171], v[192:195], v[100:103]
	v_mfma_f32_16x16x32_bf16 v[92:95], v[176:179], v[192:195], v[92:95]
	v_mfma_f32_16x16x32_bf16 v[84:87], v[168:171], v[200:203], v[84:87]
	v_mfma_f32_16x16x32_bf16 v[76:79], v[176:179], v[200:203], v[76:79]
	v_mfma_f32_16x16x32_bf16 v[68:71], v[168:171], v[208:211], v[68:71]
	v_mfma_f32_16x16x32_bf16 v[64:67], v[176:179], v[208:211], v[64:67]
	v_mfma_f32_16x16x32_bf16 v[116:119], v[172:175], v[188:191], v[116:119]
	v_mfma_f32_16x16x32_bf16 v[108:111], v[180:183], v[188:191], v[108:111]
	v_mfma_f32_16x16x32_bf16 v[100:103], v[172:175], v[196:199], v[100:103]
	v_mfma_f32_16x16x32_bf16 v[92:95], v[180:183], v[196:199], v[92:95]
	v_mfma_f32_16x16x32_bf16 v[84:87], v[172:175], v[204:207], v[84:87]
	v_mfma_f32_16x16x32_bf16 v[76:79], v[180:183], v[204:207], v[76:79]
	v_mfma_f32_16x16x32_bf16 v[68:71], v[172:175], v[212:215], v[68:71]
	v_mfma_f32_16x16x32_bf16 v[64:67], v[180:183], v[212:215], v[64:67]
	s_setprio 0
	s_barrier
; #define PG8_STAGE(bufoff, gbase, voff) do { const char* sb_ = (gbase); _Pragma("unroll") for (int _i = 0; _i < 2; ++_i) PG8_GLDS(sb_, (voff)[_i], bufoff, _i); } while (0)
; #define PG8_LDA(dst, b, h) do { if constexpr (F8) { _Pragma("unroll") for (int m = 0; m < 4; ++m) dst##8[m] = PG8_RD8(lds + PG8_SA(b, h) + aoff + m * 2048); } else { \
;         _Pragma("unroll") for (int m = 0; m < 4; ++m) _Pragma("unroll") for (int k = 0; k < 2; ++k) dst[m][k] = *(const PG8_LAS bf16x8*)(lds + PG8_SA(b, h) + aoff + m * 2048 + k * 1024); } } while (0)
; #define PG8_LDB(dst, b, h) do { if constexpr (F8) { _Pragma("unroll") for (int n = 0; n < 2; ++n) dst##8[n] = PG8_RD8(lds + PG8_SB(b, h) + boff + n * 2048); } else { \
;         _Pragma("unroll") for (int n = 0; n < 2; ++n) _Pragma("unroll") for (int k = 0; k < 2; ++k) dst[n][k] = *(const PG8_LAS bf16x8*)(lds + PG8_SB(b, h) + boff + n * 2048 + k * 1024); } } while (0)
; #define PG8_WAIT_V(n) asm volatile("s_waitcnt vmcnt(" #n ")" ::: "memory")
;     ...
;         for (int t = 0; t < nt; t += 2) {
;             const bool last = (t == nt - 2);
;             const size_t k1 = (size_t)(t + 1) * kstep;
;             const size_t k2 = last ? 0 : (size_t)(t + 2) * kstep, k3 = k2 + kstep;
;             const char* b2 = last ? nB : cB + (size_t)(t + 2) * kstep; const char* b3 = b2 + kstep;
;             PG8_LDB(B0, 0, 0); PG8_LDB(B1, 0, 1); PG8_SCHED; PG8_LDA(At, 0, 0); PG8_STAGE_A(PG8_SA(1, 1), 1, k1, false);
;             PG8_WAIT_V(8); PG8_WAIT_L(0); PG8_BAR; PG8_MMA(0, 0, At, B0); PG8_MMA(0, 1, At, B1); PG8_BAR; PG8_SCHED;
;             PG8_LDA(At, 0, 1); PG8_STAGE(PG8_SB(0, 0), b2, voffB); PG8_STAGE(PG8_SB(0, 1), b2 + hstep, voffB); PG8_STAGE_A(PG8_SA(0, 0), 0, k2, last);
;             PG8_WAIT_V(8); PG8_WAIT_L(0); PG8_BAR; PG8_MMA(1, 0, At, B0); PG8_MMA(1, 1, At, B1); PG8_BAR; PG8_SCHED;
;             PG8_LDB(B0, 1, 0); PG8_LDB(B1, 1, 1); PG8_SCHED; PG8_LDA(At, 1, 0); PG8_STAGE_A(PG8_SA(0, 1), 1, k2, last);
;             PG8_WAIT_V(8); PG8_WAIT_L(0); PG8_BAR; PG8_MMA(0, 0, At, B0); PG8_MMA(0, 1, At, B1); PG8_BAR; PG8_SCHED;
;             PG8_LDA(At, 1, 1); PG8_STAGE(PG8_SB(1, 0), b3, voffB); PG8_STAGE(PG8_SB(1, 1), b3 + hstep, voffB); PG8_STAGE_A(PG8_SA(1, 0), 0, k3, last);
;             PG8_WAIT_V(8); PG8_WAIT_L(0); PG8_BAR; PG8_MMA(1, 0, At, B0); PG8_MMA(1, 1, At, B1); PG8_BAR; PG8_SCHED;
;         }
	s_add_i32 s34, s40, s57
	v_lshl_add_u64 v[216:217], v[216:217], 0, s[8:9]
	s_mov_b32 m0, s34
	ds_read_b128 v[184:187], v151 offset:49152
	ds_read_b128 v[188:191], v151 offset:50176
	ds_read_b128 v[192:195], v151 offset:51200
	ds_read_b128 v[196:199], v151 offset:52224
	ds_read_b128 v[200:203], v151 offset:53248
	ds_read_b128 v[204:207], v151 offset:54272
	ds_read_b128 v[208:211], v151 offset:55296
	ds_read_b128 v[212:215], v151 offset:56320
	global_load_lds_dwordx4 v[216:217], off
	s_add_i32 m0, s34, 0x2000
	s_add_u32 s34, s38, 0x80080
	v_lshl_add_u64 v[216:217], v[218:219], 0, s[8:9]
	s_addc_u32 s35, s39, 0
	s_add_i32 s38, s41, s57
	global_load_lds_dwordx4 v[216:217], off
	v_lshl_add_u64 v[216:217], s[34:35], 0, v[130:131]
	s_mov_b32 m0, s38
	s_nop 0
	global_load_lds_dwordx4 v[216:217], off
	v_lshl_add_u64 v[216:217], s[34:35], 0, v[134:135]
	s_add_i32 m0, s38, 0x2000
	s_nop 0
	global_load_lds_dwordx4 v[216:217], off
	v_lshl_add_u64 v[216:217], v[220:221], 0, s[8:9]
	s_mov_b32 m0, s64
	s_nop 0
	global_load_lds_dwordx4 v[216:217], off
	v_lshl_add_u64 v[216:217], v[222:223], 0, s[8:9]
	s_mov_b32 m0, s65
	s_nop 0
	global_load_lds_dwordx4 v[216:217], off
	s_waitcnt vmcnt(8)
	s_waitcnt lgkmcnt(0)
	s_barrier
	s_setprio 1
	v_mfma_f32_16x16x32_bf16 v[60:63], v[152:155], v[184:187], v[60:63]
	v_mfma_f32_16x16x32_bf16 v[56:59], v[160:163], v[184:187], v[56:59]
	v_mfma_f32_16x16x32_bf16 v[52:55], v[152:155], v[192:195], v[52:55]
	v_mfma_f32_16x16x32_bf16 v[44:47], v[160:163], v[192:195], v[44:47]
	v_mfma_f32_16x16x32_bf16 v[36:39], v[152:155], v[200:203], v[36:39]
	v_mfma_f32_16x16x32_bf16 v[28:31], v[160:163], v[200:203], v[28:31]
	v_mfma_f32_16x16x32_bf16 v[20:23], v[152:155], v[208:211], v[20:23]
	v_mfma_f32_16x16x32_bf16 v[12:15], v[160:163], v[208:211], v[12:15]
	v_mfma_f32_16x16x32_bf16 v[60:63], v[156:159], v[188:191], v[60:63]
	v_mfma_f32_16x16x32_bf16 v[56:59], v[164:167], v[188:191], v[56:59]
	v_mfma_f32_16x16x32_bf16 v[52:55], v[156:159], v[196:199], v[52:55]
	v_mfma_f32_16x16x32_bf16 v[44:47], v[164:167], v[196:199], v[44:47]
	v_mfma_f32_16x16x32_bf16 v[36:39], v[156:159], v[204:207], v[36:39]
	v_mfma_f32_16x16x32_bf16 v[28:31], v[164:167], v[204:207], v[28:31]
	v_mfma_f32_16x16x32_bf16 v[20:23], v[156:159], v[212:215], v[20:23]
	v_mfma_f32_16x16x32_bf16 v[12:15], v[164:167], v[212:215], v[12:15]
	v_mfma_f32_16x16x32_bf16 v[48:51], v[168:171], v[184:187], v[48:51]
	v_mfma_f32_16x16x32_bf16 v[40:43], v[176:179], v[184:187], v[40:43]
	v_mfma_f32_16x16x32_bf16 v[32:35], v[168:171], v[192:195], v[32:35]
	v_mfma_f32_16x16x32_bf16 v[24:27], v[176:179], v[192:195], v[24:27]
	v_mfma_f32_16x16x32_bf16 v[16:19], v[168:171], v[200:203], v[16:19]
	v_mfma_f32_16x16x32_bf16 v[8:11], v[176:179], v[200:203], v[8:11]
	v_mfma_f32_16x16x32_bf16 v[4:7], v[168:171], v[208:211], v[4:7]
	v_mfma_f32_16x16x32_bf16 v[0:3], v[176:179], v[208:211], v[0:3]
	v_mfma_f32_16x16x32_bf16 v[48:51], v[172:175], v[188:191], v[48:51]
	v_mfma_f32_16x16x32_bf16 v[40:43], v[180:183], v[188:191], v[40:43]
	v_mfma_f32_16x16x32_bf16 v[32:35], v[172:175], v[196:199], v[32:35]
	v_mfma_f32_16x16x32_bf16 v[24:27], v[180:183], v[196:199], v[24:27]
	v_mfma_f32_16x16x32_bf16 v[16:19], v[172:175], v[204:207], v[16:19]
	v_mfma_f32_16x16x32_bf16 v[8:11], v[180:183], v[204:207], v[8:11]
	v_mfma_f32_16x16x32_bf16 v[4:7], v[172:175], v[212:215], v[4:7]
	v_mfma_f32_16x16x32_bf16 v[0:3], v[180:183], v[212:215], v[0:3]
	s_setprio 0
	s_barrier
	s_add_i32 s79, s79, 2
	s_cmp_gt_u32 s79, 29
	s_mov_b64 s[34:35], s[36:37]
	s_cbranch_scc0 .LBB4_1055
	s_and_b64 vcc, exec, s[10:11]
	s_cbranch_vccz .LBB4_1058
	s_barrier

; #define PG8_STAGE(bufoff, gbase, voff) do { const char* sb_ = (gbase); _Pragma("unroll") for (int _i = 0; _i < 2; ++_i) PG8_GLDS(sb_, (voff)[_i], bufoff, _i); } while (0)
; #define PG8_LDA(dst, b, h) do { if constexpr (F8) { _Pragma("unroll") for (int m = 0; m < 4; ++m) dst##8[m] = PG8_RD8(lds + PG8_SA(b, h) + aoff + m * 2048); } else { \
;         _Pragma("unroll") for (int m = 0; m < 4; ++m) _Pragma("unroll") for (int k = 0; k < 2; ++k) dst[m][k] = *(const PG8_LAS bf16x8*)(lds + PG8_SA(b, h) + aoff + m * 2048 + k * 1024); } } while (0)
; #define PG8_LDB(dst, b, h) do { if constexpr (F8) { _Pragma("unroll") for (int n = 0; n < 2; ++n) dst##8[n] = PG8_RD8(lds + PG8_SB(b, h) + boff + n * 2048); } else { \
;         _Pragma("unroll") for (int n = 0; n < 2; ++n) _Pragma("unroll") for (int k = 0; k < 2; ++k) dst[n][k] = *(const PG8_LAS bf16x8*)(lds + PG8_SB(b, h) + boff + n * 2048 + k * 1024); } } while (0)
; #define PG8_WAIT_V(n) asm volatile("s_waitcnt vmcnt(" #n ")" ::: "memory")
;     ...
;         for (int t = 0; t < nt; t += 2) {
;             const bool last = (t == nt - 2);
;             const size_t k1 = (size_t)(t + 1) * kstep;
;             const size_t k2 = last ? 0 : (size_t)(t + 2) * kstep, k3 = k2 + kstep;
;             const char* b2 = last ? nB : cB + (size_t)(t + 2) * kstep; const char* b3 = b2 + kstep;
;             PG8_LDB(B0, 0, 0); PG8_LDB(B1, 0, 1); PG8_SCHED; PG8_LDA(At, 0, 0); PG8_STAGE_A(PG8_SA(1, 1), 1, k1, false);
;             PG8_WAIT_V(8); PG8_WAIT_L(0); PG8_BAR; PG8_MMA(0, 0, At, B0); PG8_MMA(0, 1, At, B1); PG8_BAR; PG8_SCHED;
;             PG8_LDA(At, 0, 1); PG8_STAGE(PG8_SB(0, 0), b2, voffB); PG8_STAGE(PG8_SB(0, 1), b2 + hstep, voffB); PG8_STAGE_A(PG8_SA(0, 0), 0, k2, last);
;             PG8_WAIT_V(8); PG8_WAIT_L(0); PG8_BAR; PG8_MMA(1, 0, At, B0); PG8_MMA(1, 1, At, B1); PG8_BAR; PG8_SCHED;
;             PG8_LDB(B0, 1, 0); PG8_LDB(B1, 1, 1); PG8_SCHED; PG8_LDA(At, 1, 0); PG8_STAGE_A(PG8_SA(0, 1), 1, k2, last);
;             PG8_WAIT_V(8); PG8_WAIT_L(0); PG8_BAR; PG8_MMA(0, 0, At, B0); PG8_MMA(0, 1, At, B1); PG8_BAR; PG8_SCHED;
;             PG8_LDA(At, 1, 1); PG8_STAGE(PG8_SB(1, 0), b3, voffB); PG8_STAGE(PG8_SB(1, 1), b3 + hstep, voffB); PG8_STAGE_A(PG8_SA(1, 0), 0, k3, last);
;             PG8_WAIT_V(8); PG8_WAIT_L(0); PG8_BAR; PG8_MMA(1, 0, At, B0); PG8_MMA(1, 1, At, B1); PG8_BAR; PG8_SCHED;
;         }
.LBB4_1452:
	ds_read_b128 v[146:149], v138
	ds_read_b128 v[150:153], v138 offset:16
	ds_read_b128 v[154:157], v138 offset:2048
	ds_read_b128 v[158:161], v138 offset:2064
	ds_read_b128 v[162:165], v139
	ds_read_b128 v[166:169], v139 offset:16
	ds_read_b128 v[170:173], v139 offset:2048
	ds_read_b128 v[174:177], v139 offset:2064
	s_add_u32 s28, s20, s24
	s_addc_u32 s29, s21, s25
	s_cmp_eq_u32 s15, 12
	s_cselect_b64 s[30:31], -1, 0
	s_and_b64 s[26:27], s[30:31], exec
	s_cselect_b32 s82, 0, s24
	s_cselect_b32 s27, s17, s29
	s_cselect_b32 s26, s16, s28
	ds_read_b128 v[178:181], v140
	ds_read_b128 v[182:185], v140 offset:16
	ds_read_b128 v[186:189], v140 offset:2048
	ds_read_b128 v[190:193], v140 offset:2064
	ds_read_b128 v[194:197], v140 offset:4096
	ds_read_b128 v[198:201], v140 offset:4112
	ds_read_b128 v[202:205], v140 offset:6144
	ds_read_b128 v[206:209], v140 offset:6160
	ds_read2st64_b32 v[128:129], v132 offset0:16 offset1:24
	s_add_u32 s28, s6, s24
	s_addc_u32 s29, s7, s25
	s_add_u32 s28, s28, 0xffffff80
	s_addc_u32 s29, s29, -1
	s_waitcnt lgkmcnt(0)
	s_mov_b32 m0, s66
	s_nop 0
	global_load_lds_dwordx4 v128, s[28:29]
	s_nop 0
	s_mov_b32 m0, s67
	s_nop 0
	global_load_lds_dwordx4 v129, s[28:29]
	s_waitcnt vmcnt(8)
	s_waitcnt lgkmcnt(0)
	s_barrier
	s_setprio 1
	v_mfma_scale_f32_16x16x128_f8f6f4 v[124:127], v[146:153], v[178:185], v[124:127], v142, v141 op_sel_hi:[0,0,0]
	v_mfma_scale_f32_16x16x128_f8f6f4 v[120:123], v[154:161], v[178:185], v[120:123], v142, v141 op_sel_hi:[0,0,0]
	v_mfma_scale_f32_16x16x128_f8f6f4 v[108:111], v[146:153], v[186:193], v[108:111], v142, v141 op_sel_hi:[0,0,0]
	v_mfma_scale_f32_16x16x128_f8f6f4 v[104:107], v[154:161], v[186:193], v[104:107], v142, v141 op_sel_hi:[0,0,0]
	v_mfma_scale_f32_16x16x128_f8f6f4 v[210:213], v[146:153], v[194:201], v[92:95], v142, v141 op_sel_hi:[0,0,0]
	v_mfma_scale_f32_16x16x128_f8f6f4 v[214:217], v[154:161], v[194:201], v[88:91], v142, v141 op_sel_hi:[0,0,0]
	v_mfma_scale_f32_16x16x128_f8f6f4 v[218:221], v[146:153], v[202:209], v[76:79], v142, v141 op_sel_hi:[0,0,0]
	v_mfma_scale_f32_16x16x128_f8f6f4 v[222:225], v[154:161], v[202:209], v[72:75], v142, v141 op_sel_hi:[0,0,0]
	v_mfma_scale_f32_16x16x128_f8f6f4 v[116:119], v[162:169], v[178:185], v[116:119], v142, v141 op_sel_hi:[0,0,0]
	v_mfma_scale_f32_16x16x128_f8f6f4 v[112:115], v[170:177], v[178:185], v[112:115], v142, v141 op_sel_hi:[0,0,0]
	v_mfma_scale_f32_16x16x128_f8f6f4 v[100:103], v[162:169], v[186:193], v[100:103], v142, v141 op_sel_hi:[0,0,0]
	v_mfma_scale_f32_16x16x128_f8f6f4 v[96:99], v[170:177], v[186:193], v[96:99], v142, v141 op_sel_hi:[0,0,0]
	v_mfma_scale_f32_16x16x128_f8f6f4 v[178:181], v[162:169], v[194:201], v[84:87], v142, v141 op_sel_hi:[0,0,0]
	v_mfma_scale_f32_16x16x128_f8f6f4 v[182:185], v[170:177], v[194:201], v[80:83], v142, v141 op_sel_hi:[0,0,0]
	v_mfma_scale_f32_16x16x128_f8f6f4 v[186:189], v[162:169], v[202:209], v[68:71], v142, v141 op_sel_hi:[0,0,0]
	v_mfma_scale_f32_16x16x128_f8f6f4 v[190:193], v[170:177], v[202:209], v[64:67], v142, v141 op_sel_hi:[0,0,0]
	s_setprio 0
	s_barrier
	s_nop 4
	ds_read_b128 v[64:67], v140 offset:16384
	ds_read_b128 v[68:71], v140 offset:16400
	ds_read_b128 v[72:75], v140 offset:18432
	ds_read_b128 v[76:79], v140 offset:18448
	ds_read_b128 v[80:83], v140 offset:20480
	ds_read_b128 v[84:87], v140 offset:20496
	ds_read_b128 v[88:91], v140 offset:22528
	ds_read_b128 v[92:95], v140 offset:22544
	s_mov_b32 m0, s19
	s_nop 0
	global_load_lds_dwordx4 v135, s[26:27]
	s_add_u32 s28, s26, 0x40000
	s_mov_b32 m0, s42
	s_nop 0
	global_load_lds_dwordx4 v136, s[26:27]
	s_addc_u32 s29, s27, 0
	s_mov_b32 m0, s43
	s_nop 0
	global_load_lds_dwordx4 v135, s[28:29]
	s_nop 0
	s_mov_b32 m0, s54
	s_nop 0
	global_load_lds_dwordx4 v136, s[28:29]
	s_add_u32 s28, s6, s82
	s_addc_u32 s29, s7, 0
	s_and_b64 s[30:31], s[22:23], s[30:31]
	s_and_b64 s[30:31], s[30:31], exec
	s_cselect_b32 s30, s78, s80
	s_lshl_b32 s30, s30, 13
	s_and_b32 s30, s30, 0x2000
	v_add_u32_e32 v133, s30, v137
	ds_read2st64_b32 v[128:129], v133 offset1:8
	s_waitcnt lgkmcnt(0)
	s_mov_b32 m0, s39
	s_nop 0
	global_load_lds_dwordx4 v128, s[28:29]
	s_nop 0
	s_mov_b32 m0, s55
	s_nop 0
	global_load_lds_dwordx4 v129, s[28:29]
	s_waitcnt vmcnt(8)
	s_waitcnt lgkmcnt(0)
	s_barrier
	s_setprio 1
	v_mfma_scale_f32_16x16x128_f8f6f4 v[60:63], v[146:153], v[64:71], v[60:63], v142, v141 op_sel_hi:[0,0,0]
	v_mfma_scale_f32_16x16x128_f8f6f4 v[56:59], v[154:161], v[64:71], v[56:59], v142, v141 op_sel_hi:[0,0,0]
	v_mfma_scale_f32_16x16x128_f8f6f4 v[194:197], v[146:153], v[72:79], v[44:47], v142, v141 op_sel_hi:[0,0,0]
	v_mfma_scale_f32_16x16x128_f8f6f4 v[198:201], v[154:161], v[72:79], v[40:43], v142, v141 op_sel_hi:[0,0,0]
	v_mfma_scale_f32_16x16x128_f8f6f4 v[202:205], v[146:153], v[80:87], v[28:31], v142, v141 op_sel_hi:[0,0,0]
	v_mfma_scale_f32_16x16x128_f8f6f4 v[206:209], v[154:161], v[80:87], v[24:27], v142, v141 op_sel_hi:[0,0,0]
	v_mfma_scale_f32_16x16x128_f8f6f4 v[226:229], v[146:153], v[88:95], v[12:15], v142, v141 op_sel_hi:[0,0,0]
	v_mfma_scale_f32_16x16x128_f8f6f4 v[230:233], v[154:161], v[88:95], v[8:11], v142, v141 op_sel_hi:[0,0,0]
	v_mfma_scale_f32_16x16x128_f8f6f4 v[52:55], v[162:169], v[64:71], v[52:55], v142, v141 op_sel_hi:[0,0,0]
	v_mfma_scale_f32_16x16x128_f8f6f4 v[48:51], v[170:177], v[64:71], v[48:51], v142, v141 op_sel_hi:[0,0,0]
	v_mfma_scale_f32_16x16x128_f8f6f4 v[234:237], v[162:169], v[72:79], v[36:39], v142, v141 op_sel_hi:[0,0,0]
	v_mfma_scale_f32_16x16x128_f8f6f4 v[238:241], v[170:177], v[72:79], v[32:35], v142, v141 op_sel_hi:[0,0,0]
	v_mfma_scale_f32_16x16x128_f8f6f4 v[242:245], v[162:169], v[80:87], v[20:23], v142, v141 op_sel_hi:[0,0,0]
	v_mfma_scale_f32_16x16x128_f8f6f4 v[246:249], v[170:177], v[80:87], v[16:19], v142, v141 op_sel_hi:[0,0,0]
	v_mfma_scale_f32_16x16x128_f8f6f4 v[250:253], v[162:169], v[88:95], v[4:7], v142, v141 op_sel_hi:[0,0,0]
	v_mfma_scale_f32_16x16x128_f8f6f4 v[128:131], v[170:177], v[88:95], v[0:3], v142, v141 op_sel_hi:[0,0,0]
	s_setprio 0
	s_barrier
; #define PG8_STAGE(bufoff, gbase, voff) do { const char* sb_ = (gbase); _Pragma("unroll") for (int _i = 0; _i < 2; ++_i) PG8_GLDS(sb_, (voff)[_i], bufoff, _i); } while (0)
; #define PG8_LDA(dst, b, h) do { if constexpr (F8) { _Pragma("unroll") for (int m = 0; m < 4; ++m) dst##8[m] = PG8_RD8(lds + PG8_SA(b, h) + aoff + m * 2048); } else { \
;         _Pragma("unroll") for (int m = 0; m < 4; ++m) _Pragma("unroll") for (int k = 0; k < 2; ++k) dst[m][k] = *(const PG8_LAS bf16x8*)(lds + PG8_SA(b, h) + aoff + m * 2048 + k * 1024); } } while (0)
; #define PG8_LDB(dst, b, h) do { if constexpr (F8) { _Pragma("unroll") for (int n = 0; n < 2; ++n) dst##8[n] = PG8_RD8(lds + PG8_SB(b, h) + boff + n * 2048); } else { \
;         _Pragma("unroll") for (int n = 0; n < 2; ++n) _Pragma("unroll") for (int k = 0; k < 2; ++k) dst[n][k] = *(const PG8_LAS bf16x8*)(lds + PG8_SB(b, h) + boff + n * 2048 + k * 1024); } } while (0)
; #define PG8_WAIT_V(n) asm volatile("s_waitcnt vmcnt(" #n ")" ::: "memory")
;     ...
;         for (int t = 0; t < nt; t += 2) {
;             const bool last = (t == nt - 2);
;             const size_t k1 = (size_t)(t + 1) * kstep;
;             const size_t k2 = last ? 0 : (size_t)(t + 2) * kstep, k3 = k2 + kstep;
;             const char* b2 = last ? nB : cB + (size_t)(t + 2) * kstep; const char* b3 = b2 + kstep;
;             PG8_LDB(B0, 0, 0); PG8_LDB(B1, 0, 1); PG8_SCHED; PG8_LDA(At, 0, 0); PG8_STAGE_A(PG8_SA(1, 1), 1, k1, false);
;             PG8_WAIT_V(8); PG8_WAIT_L(0); PG8_BAR; PG8_MMA(0, 0, At, B0); PG8_MMA(0, 1, At, B1); PG8_BAR; PG8_SCHED;
;             PG8_LDA(At, 0, 1); PG8_STAGE(PG8_SB(0, 0), b2, voffB); PG8_STAGE(PG8_SB(0, 1), b2 + hstep, voffB); PG8_STAGE_A(PG8_SA(0, 0), 0, k2, last);
;             PG8_WAIT_V(8); PG8_WAIT_L(0); PG8_BAR; PG8_MMA(1, 0, At, B0); PG8_MMA(1, 1, At, B1); PG8_BAR; PG8_SCHED;
;             PG8_LDB(B0, 1, 0); PG8_LDB(B1, 1, 1); PG8_SCHED; PG8_LDA(At, 1, 0); PG8_STAGE_A(PG8_SA(0, 1), 1, k2, last);
;             PG8_WAIT_V(8); PG8_WAIT_L(0); PG8_BAR; PG8_MMA(0, 0, At, B0); PG8_MMA(0, 1, At, B1); PG8_BAR; PG8_SCHED;
;             PG8_LDA(At, 1, 1); PG8_STAGE(PG8_SB(1, 0), b3, voffB); PG8_STAGE(PG8_SB(1, 1), b3 + hstep, voffB); PG8_STAGE_A(PG8_SA(1, 0), 0, k3, last);
;             PG8_WAIT_V(8); PG8_WAIT_L(0); PG8_BAR; PG8_MMA(1, 0, At, B0); PG8_MMA(1, 1, At, B1); PG8_BAR; PG8_SCHED;
;         }
	s_nop 4
	ds_read_b128 v[0:3], v143
	ds_read_b128 v[4:7], v143 offset:16
	ds_read_b128 v[16:19], v143 offset:2048
	ds_read_b128 v[20:23], v143 offset:2064
	ds_read_b128 v[146:149], v144
	ds_read_b128 v[150:153], v144 offset:16
	ds_read_b128 v[154:157], v144 offset:2048
	ds_read_b128 v[158:161], v144 offset:2064
	ds_read_b128 v[8:11], v140 offset:32768
	ds_read_b128 v[12:15], v140 offset:32784
	ds_read_b128 v[24:27], v140 offset:34816
	ds_read_b128 v[28:31], v140 offset:34832
	ds_read2st64_b32 v[64:65], v133 offset0:16 offset1:24
	ds_read_b128 v[32:35], v140 offset:36864
	ds_read_b128 v[36:39], v140 offset:36880
	ds_read_b128 v[40:43], v140 offset:38912
	ds_read_b128 v[44:47], v140 offset:38928
	s_waitcnt lgkmcnt(4)
	s_mov_b32 m0, s56
	s_nop 0
	global_load_lds_dwordx4 v64, s[28:29]
	s_nop 0
	s_mov_b32 m0, s57
	s_nop 0
	global_load_lds_dwordx4 v65, s[28:29]
	s_waitcnt vmcnt(8)
	s_waitcnt lgkmcnt(0)
	s_barrier
	s_setprio 1
	v_mfma_scale_f32_16x16x128_f8f6f4 v[124:127], v[0:7], v[8:15], v[124:127], v142, v141 op_sel_hi:[0,0,0]
	v_mfma_scale_f32_16x16x128_f8f6f4 v[120:123], v[16:23], v[8:15], v[120:123], v142, v141 op_sel_hi:[0,0,0]
	v_mfma_scale_f32_16x16x128_f8f6f4 v[108:111], v[0:7], v[24:31], v[108:111], v142, v141 op_sel_hi:[0,0,0]
	v_mfma_scale_f32_16x16x128_f8f6f4 v[104:107], v[16:23], v[24:31], v[104:107], v142, v141 op_sel_hi:[0,0,0]
	v_mfma_scale_f32_16x16x128_f8f6f4 v[92:95], v[0:7], v[32:39], v[210:213], v142, v141 op_sel_hi:[0,0,0]
	v_mfma_scale_f32_16x16x128_f8f6f4 v[88:91], v[16:23], v[32:39], v[214:217], v142, v141 op_sel_hi:[0,0,0]
	v_mfma_scale_f32_16x16x128_f8f6f4 v[76:79], v[0:7], v[40:47], v[218:221], v142, v141 op_sel_hi:[0,0,0]
	v_mfma_scale_f32_16x16x128_f8f6f4 v[72:75], v[16:23], v[40:47], v[222:225], v142, v141 op_sel_hi:[0,0,0]
	v_mfma_scale_f32_16x16x128_f8f6f4 v[116:119], v[146:153], v[8:15], v[116:119], v142, v141 op_sel_hi:[0,0,0]
	v_mfma_scale_f32_16x16x128_f8f6f4 v[112:115], v[154:161], v[8:15], v[112:115], v142, v141 op_sel_hi:[0,0,0]
	v_mfma_scale_f32_16x16x128_f8f6f4 v[100:103], v[146:153], v[24:31], v[100:103], v142, v141 op_sel_hi:[0,0,0]
	v_mfma_scale_f32_16x16x128_f8f6f4 v[96:99], v[154:161], v[24:31], v[96:99], v142, v141 op_sel_hi:[0,0,0]
	v_mfma_scale_f32_16x16x128_f8f6f4 v[84:87], v[146:153], v[32:39], v[178:181], v142, v141 op_sel_hi:[0,0,0]
	v_mfma_scale_f32_16x16x128_f8f6f4 v[80:83], v[154:161], v[32:39], v[182:185], v142, v141 op_sel_hi:[0,0,0]
	v_mfma_scale_f32_16x16x128_f8f6f4 v[68:71], v[146:153], v[40:47], v[186:189], v142, v141 op_sel_hi:[0,0,0]
	v_mfma_scale_f32_16x16x128_f8f6f4 v[64:67], v[154:161], v[40:47], v[190:193], v142, v141 op_sel_hi:[0,0,0]
	s_setprio 0
	s_barrier
	ds_read_b128 v[32:35], v140 offset:49152
	ds_read_b128 v[36:39], v140 offset:49168
	ds_read_b128 v[162:165], v140 offset:51200
	ds_read_b128 v[166:169], v140 offset:51216
	ds_read_b128 v[170:173], v140 offset:53248
	ds_read_b128 v[174:177], v140 offset:53264
	ds_read_b128 v[178:181], v140 offset:55296
	ds_read_b128 v[182:185], v140 offset:55312
	s_add_u32 s30, s26, 0x80
	s_addc_u32 s31, s27, 0
	s_mov_b32 m0, s60
	s_nop 0
	global_load_lds_dwordx4 v135, s[30:31]
	s_add_u32 s26, s26, 0x40080
	s_mov_b32 m0, s61
	s_nop 0
	global_load_lds_dwordx4 v136, s[30:31]
	s_addc_u32 s27, s27, 0
	s_mov_b32 m0, s64
	s_nop 0
	global_load_lds_dwordx4 v135, s[26:27]
	s_nop 0
	s_mov_b32 m0, s65
	s_nop 0
	global_load_lds_dwordx4 v136, s[26:27]
	s_add_u32 s26, s28, 0x80
	ds_read2st64_b32 v[8:9], v133 offset1:8
	s_addc_u32 s27, s29, 0
	s_waitcnt lgkmcnt(0)
	s_mov_b32 m0, s62
	s_nop 0
	global_load_lds_dwordx4 v8, s[26:27]
	s_nop 0
	s_mov_b32 m0, s63
	s_nop 0
	global_load_lds_dwordx4 v9, s[26:27]
	s_waitcnt vmcnt(8)
	s_waitcnt lgkmcnt(0)
	s_barrier
	s_setprio 1
	v_mfma_scale_f32_16x16x128_f8f6f4 v[60:63], v[0:7], v[32:39], v[60:63], v142, v141 op_sel_hi:[0,0,0]
	v_mfma_scale_f32_16x16x128_f8f6f4 v[56:59], v[16:23], v[32:39], v[56:59], v142, v141 op_sel_hi:[0,0,0]
	v_mfma_scale_f32_16x16x128_f8f6f4 v[44:47], v[0:7], v[162:169], v[194:197], v142, v141 op_sel_hi:[0,0,0]
	v_mfma_scale_f32_16x16x128_f8f6f4 v[40:43], v[16:23], v[162:169], v[198:201], v142, v141 op_sel_hi:[0,0,0]
	v_mfma_scale_f32_16x16x128_f8f6f4 v[28:31], v[0:7], v[170:177], v[202:205], v142, v141 op_sel_hi:[0,0,0]
	v_mfma_scale_f32_16x16x128_f8f6f4 v[24:27], v[16:23], v[170:177], v[206:209], v142, v141 op_sel_hi:[0,0,0]
	v_mfma_scale_f32_16x16x128_f8f6f4 v[12:15], v[0:7], v[178:185], v[226:229], v142, v141 op_sel_hi:[0,0,0]
	v_mfma_scale_f32_16x16x128_f8f6f4 v[8:11], v[16:23], v[178:185], v[230:233], v142, v141 op_sel_hi:[0,0,0]
	v_mfma_scale_f32_16x16x128_f8f6f4 v[52:55], v[146:153], v[32:39], v[52:55], v142, v141 op_sel_hi:[0,0,0]
	v_mfma_scale_f32_16x16x128_f8f6f4 v[48:51], v[154:161], v[32:39], v[48:51], v142, v141 op_sel_hi:[0,0,0]
	v_mfma_scale_f32_16x16x128_f8f6f4 v[36:39], v[146:153], v[162:169], v[234:237], v142, v141 op_sel_hi:[0,0,0]
	v_mfma_scale_f32_16x16x128_f8f6f4 v[32:35], v[154:161], v[162:169], v[238:241], v142, v141 op_sel_hi:[0,0,0]
	v_mfma_scale_f32_16x16x128_f8f6f4 v[20:23], v[146:153], v[170:177], v[242:245], v142, v141 op_sel_hi:[0,0,0]
	v_mfma_scale_f32_16x16x128_f8f6f4 v[16:19], v[154:161], v[170:177], v[246:249], v142, v141 op_sel_hi:[0,0,0]
	v_mfma_scale_f32_16x16x128_f8f6f4 v[4:7], v[146:153], v[178:185], v[250:253], v142, v141 op_sel_hi:[0,0,0]
	v_mfma_scale_f32_16x16x128_f8f6f4 v[0:3], v[154:161], v[178:185], v[128:131], v142, v141 op_sel_hi:[0,0,0]
	s_setprio 0
	s_barrier
	s_add_i32 s15, s15, 2
	s_add_u32 s24, s24, 0x100
	s_addc_u32 s25, s25, 0
	s_cmp_gt_u32 s15, 13
	s_cbranch_scc0 .LBB4_1452
	s_and_b64 vcc, exec, s[12:13]
	s_cbranch_vccz .LBB4_1455
	s_barrier

; #define PG8_STAGE(bufoff, gbase, voff) do { const char* sb_ = (gbase); _Pragma("unroll") for (int _i = 0; _i < 2; ++_i) PG8_GLDS(sb_, (voff)[_i], bufoff, _i); } while (0)
; #define PG8_LDA(dst, b, h) do { if constexpr (F8) { _Pragma("unroll") for (int m = 0; m < 4; ++m) dst##8[m] = PG8_RD8(lds + PG8_SA(b, h) + aoff + m * 2048); } else { \
;         _Pragma("unroll") for (int m = 0; m < 4; ++m) _Pragma("unroll") for (int k = 0; k < 2; ++k) dst[m][k] = *(const PG8_LAS bf16x8*)(lds + PG8_SA(b, h) + aoff + m * 2048 + k * 1024); } } while (0)
; #define PG8_LDB(dst, b, h) do { if constexpr (F8) { _Pragma("unroll") for (int n = 0; n < 2; ++n) dst##8[n] = PG8_RD8(lds + PG8_SB(b, h) + boff + n * 2048); } else { \
;         _Pragma("unroll") for (int n = 0; n < 2; ++n) _Pragma("unroll") for (int k = 0; k < 2; ++k) dst[n][k] = *(const PG8_LAS bf16x8*)(lds + PG8_SB(b, h) + boff + n * 2048 + k * 1024); } } while (0)
; #define PG8_WAIT_V(n) asm volatile("s_waitcnt vmcnt(" #n ")" ::: "memory")
;     ...
;         for (int t = 0; t < nt; t += 2) {
;             const bool last = (t == nt - 2);
;             const size_t k1 = (size_t)(t + 1) * kstep;
;             const size_t k2 = last ? 0 : (size_t)(t + 2) * kstep, k3 = k2 + kstep;
;             const char* b2 = last ? nB : cB + (size_t)(t + 2) * kstep; const char* b3 = b2 + kstep;
;             PG8_LDB(B0, 0, 0); PG8_LDB(B1, 0, 1); PG8_SCHED; PG8_LDA(At, 0, 0); PG8_STAGE_A(PG8_SA(1, 1), 1, k1, false);
;             PG8_WAIT_V(8); PG8_WAIT_L(0); PG8_BAR; PG8_MMA(0, 0, At, B0); PG8_MMA(0, 1, At, B1); PG8_BAR; PG8_SCHED;
;             PG8_LDA(At, 0, 1); PG8_STAGE(PG8_SB(0, 0), b2, voffB); PG8_STAGE(PG8_SB(0, 1), b2 + hstep, voffB); PG8_STAGE_A(PG8_SA(0, 0), 0, k2, last);
;             PG8_WAIT_V(8); PG8_WAIT_L(0); PG8_BAR; PG8_MMA(1, 0, At, B0); PG8_MMA(1, 1, At, B1); PG8_BAR; PG8_SCHED;
;             PG8_LDB(B0, 1, 0); PG8_LDB(B1, 1, 1); PG8_SCHED; PG8_LDA(At, 1, 0); PG8_STAGE_A(PG8_SA(0, 1), 1, k2, last);
;             PG8_WAIT_V(8); PG8_WAIT_L(0); PG8_BAR; PG8_MMA(0, 0, At, B0); PG8_MMA(0, 1, At, B1); PG8_BAR; PG8_SCHED;
;             PG8_LDA(At, 1, 1); PG8_STAGE(PG8_SB(1, 0), b3, voffB); PG8_STAGE(PG8_SB(1, 1), b3 + hstep, voffB); PG8_STAGE_A(PG8_SA(1, 0), 0, k3, last);
;             PG8_WAIT_V(8); PG8_WAIT_L(0); PG8_BAR; PG8_MMA(1, 0, At, B0); PG8_MMA(1, 1, At, B1); PG8_BAR; PG8_SCHED;
;         }
.LBB4_1541:
	ds_read_b128 v[130:133], v146
	ds_read_b128 v[134:137], v146 offset:16
	ds_read_b128 v[154:157], v146 offset:2048
	ds_read_b128 v[158:161], v146 offset:2064
	ds_read_b128 v[162:165], v147
	ds_read_b128 v[166:169], v147 offset:16
	ds_read_b128 v[170:173], v147 offset:2048
	ds_read_b128 v[174:177], v147 offset:2064
	s_add_i32 s25, s40, 0xfffc0080
	s_add_u32 s42, s38, s40
	s_addc_u32 s43, s39, s41
	s_add_u32 s42, s42, 0xfffc0080
	s_addc_u32 s43, s43, -1
	s_add_u32 s54, s36, s40
	s_addc_u32 s55, s37, s41
	s_cmp_eq_u32 s23, 12
	s_cselect_b32 s25, 0, s25
	s_cselect_b32 s43, s31, s43
	s_cselect_b32 s42, s30, s42
	ds_read_b128 v[178:181], v148
	ds_read_b128 v[182:185], v148 offset:16
	ds_read_b128 v[186:189], v148 offset:2048
	ds_read_b128 v[190:193], v148 offset:2064
	ds_read_b128 v[194:197], v148 offset:4096
	ds_read_b128 v[198:201], v148 offset:4112
	ds_read_b128 v[202:205], v148 offset:6144
	ds_read_b128 v[206:209], v148 offset:6160
	s_mov_b32 m0, s80
	s_nop 0
	global_load_lds_dwordx4 v142, s[54:55]
	s_nop 0
	s_mov_b32 m0, s86
	s_nop 0
	global_load_lds_dwordx4 v144, s[54:55]
	s_waitcnt vmcnt(8)
	s_waitcnt lgkmcnt(0)
	s_barrier
	s_setprio 1
	v_mfma_scale_f32_16x16x128_f8f6f4 v[124:127], v[130:137], v[178:185], v[124:127], v150, v149 op_sel_hi:[0,0,0]
	v_mfma_scale_f32_16x16x128_f8f6f4 v[120:123], v[154:161], v[178:185], v[120:123], v150, v149 op_sel_hi:[0,0,0]
	v_mfma_scale_f32_16x16x128_f8f6f4 v[108:111], v[130:137], v[186:193], v[108:111], v150, v149 op_sel_hi:[0,0,0]
	v_mfma_scale_f32_16x16x128_f8f6f4 v[104:107], v[154:161], v[186:193], v[104:107], v150, v149 op_sel_hi:[0,0,0]
	v_mfma_scale_f32_16x16x128_f8f6f4 v[138:141], v[130:137], v[194:201], v[92:95], v150, v149 op_sel_hi:[0,0,0]
	v_mfma_scale_f32_16x16x128_f8f6f4 v[210:213], v[154:161], v[194:201], v[88:91], v150, v149 op_sel_hi:[0,0,0]
	v_mfma_scale_f32_16x16x128_f8f6f4 v[214:217], v[130:137], v[202:209], v[76:79], v150, v149 op_sel_hi:[0,0,0]
	v_mfma_scale_f32_16x16x128_f8f6f4 v[218:221], v[154:161], v[202:209], v[72:75], v150, v149 op_sel_hi:[0,0,0]
	v_mfma_scale_f32_16x16x128_f8f6f4 v[116:119], v[162:169], v[178:185], v[116:119], v150, v149 op_sel_hi:[0,0,0]
	v_mfma_scale_f32_16x16x128_f8f6f4 v[112:115], v[170:177], v[178:185], v[112:115], v150, v149 op_sel_hi:[0,0,0]
	v_mfma_scale_f32_16x16x128_f8f6f4 v[100:103], v[162:169], v[186:193], v[100:103], v150, v149 op_sel_hi:[0,0,0]
	v_mfma_scale_f32_16x16x128_f8f6f4 v[96:99], v[170:177], v[186:193], v[96:99], v150, v149 op_sel_hi:[0,0,0]
	v_mfma_scale_f32_16x16x128_f8f6f4 v[178:181], v[162:169], v[194:201], v[84:87], v150, v149 op_sel_hi:[0,0,0]
	v_mfma_scale_f32_16x16x128_f8f6f4 v[182:185], v[170:177], v[194:201], v[80:83], v150, v149 op_sel_hi:[0,0,0]
	v_mfma_scale_f32_16x16x128_f8f6f4 v[186:189], v[162:169], v[202:209], v[68:71], v150, v149 op_sel_hi:[0,0,0]
	v_mfma_scale_f32_16x16x128_f8f6f4 v[190:193], v[170:177], v[202:209], v[64:67], v150, v149 op_sel_hi:[0,0,0]
	s_setprio 0
	s_barrier
	s_nop 4
	ds_read_b128 v[64:67], v148 offset:16384
	ds_read_b128 v[68:71], v148 offset:16400
	ds_read_b128 v[72:75], v148 offset:18432
	ds_read_b128 v[76:79], v148 offset:18448
	ds_read_b128 v[80:83], v148 offset:20480
	ds_read_b128 v[84:87], v148 offset:20496
	ds_read_b128 v[88:91], v148 offset:22528
	ds_read_b128 v[92:95], v148 offset:22544
	s_mov_b32 m0, s35
	s_nop 0
	global_load_lds_dwordx4 v143, s[42:43]
	s_cselect_b32 s89, s29, s37
	s_mov_b32 m0, s61
	s_nop 0
	global_load_lds_dwordx4 v145, s[42:43]
	s_cselect_b32 s90, s28, s36
	s_add_u32 s54, s42, 0x40000
	s_addc_u32 s55, s43, 0
	s_mov_b32 m0, s62
	s_nop 0
	global_load_lds_dwordx4 v143, s[54:55]
	s_nop 0
	s_mov_b32 m0, s63
	s_nop 0
	global_load_lds_dwordx4 v145, s[54:55]
	s_add_u32 s54, s90, s25
	s_addc_u32 s55, s89, 0
	s_mov_b32 m0, s60
	s_nop 0
	global_load_lds_dwordx4 v142, s[54:55]
	s_nop 0
	s_mov_b32 m0, s64
	s_nop 0
	global_load_lds_dwordx4 v144, s[54:55]
	s_waitcnt vmcnt(8)
	s_waitcnt lgkmcnt(0)
	s_barrier
	s_setprio 1
	v_mfma_scale_f32_16x16x128_f8f6f4 v[60:63], v[130:137], v[64:71], v[60:63], v150, v149 op_sel_hi:[0,0,0]
	v_mfma_scale_f32_16x16x128_f8f6f4 v[56:59], v[154:161], v[64:71], v[56:59], v150, v149 op_sel_hi:[0,0,0]
	v_mfma_scale_f32_16x16x128_f8f6f4 v[194:197], v[130:137], v[72:79], v[44:47], v150, v149 op_sel_hi:[0,0,0]
	v_mfma_scale_f32_16x16x128_f8f6f4 v[198:201], v[154:161], v[72:79], v[40:43], v150, v149 op_sel_hi:[0,0,0]
	v_mfma_scale_f32_16x16x128_f8f6f4 v[202:205], v[130:137], v[80:87], v[28:31], v150, v149 op_sel_hi:[0,0,0]
	v_mfma_scale_f32_16x16x128_f8f6f4 v[206:209], v[154:161], v[80:87], v[24:27], v150, v149 op_sel_hi:[0,0,0]
	v_mfma_scale_f32_16x16x128_f8f6f4 v[222:225], v[130:137], v[88:95], v[12:15], v150, v149 op_sel_hi:[0,0,0]
	v_mfma_scale_f32_16x16x128_f8f6f4 v[226:229], v[154:161], v[88:95], v[8:11], v150, v149 op_sel_hi:[0,0,0]
	v_mfma_scale_f32_16x16x128_f8f6f4 v[52:55], v[162:169], v[64:71], v[52:55], v150, v149 op_sel_hi:[0,0,0]
	v_mfma_scale_f32_16x16x128_f8f6f4 v[48:51], v[170:177], v[64:71], v[48:51], v150, v149 op_sel_hi:[0,0,0]
	v_mfma_scale_f32_16x16x128_f8f6f4 v[230:233], v[162:169], v[72:79], v[36:39], v150, v149 op_sel_hi:[0,0,0]
	v_mfma_scale_f32_16x16x128_f8f6f4 v[234:237], v[170:177], v[72:79], v[32:35], v150, v149 op_sel_hi:[0,0,0]
	v_mfma_scale_f32_16x16x128_f8f6f4 v[238:241], v[162:169], v[80:87], v[20:23], v150, v149 op_sel_hi:[0,0,0]
	v_mfma_scale_f32_16x16x128_f8f6f4 v[242:245], v[170:177], v[80:87], v[16:19], v150, v149 op_sel_hi:[0,0,0]
	v_mfma_scale_f32_16x16x128_f8f6f4 v[246:249], v[162:169], v[88:95], v[4:7], v150, v149 op_sel_hi:[0,0,0]
	v_mfma_scale_f32_16x16x128_f8f6f4 v[250:253], v[170:177], v[88:95], v[0:3], v150, v149 op_sel_hi:[0,0,0]
	s_setprio 0
	s_barrier
; #define PG8_STAGE(bufoff, gbase, voff) do { const char* sb_ = (gbase); _Pragma("unroll") for (int _i = 0; _i < 2; ++_i) PG8_GLDS(sb_, (voff)[_i], bufoff, _i); } while (0)
; #define PG8_LDA(dst, b, h) do { if constexpr (F8) { _Pragma("unroll") for (int m = 0; m < 4; ++m) dst##8[m] = PG8_RD8(lds + PG8_SA(b, h) + aoff + m * 2048); } else { \
;         _Pragma("unroll") for (int m = 0; m < 4; ++m) _Pragma("unroll") for (int k = 0; k < 2; ++k) dst[m][k] = *(const PG8_LAS bf16x8*)(lds + PG8_SA(b, h) + aoff + m * 2048 + k * 1024); } } while (0)
; #define PG8_LDB(dst, b, h) do { if constexpr (F8) { _Pragma("unroll") for (int n = 0; n < 2; ++n) dst##8[n] = PG8_RD8(lds + PG8_SB(b, h) + boff + n * 2048); } else { \
;         _Pragma("unroll") for (int n = 0; n < 2; ++n) _Pragma("unroll") for (int k = 0; k < 2; ++k) dst[n][k] = *(const PG8_LAS bf16x8*)(lds + PG8_SB(b, h) + boff + n * 2048 + k * 1024); } } while (0)
; #define PG8_WAIT_V(n) asm volatile("s_waitcnt vmcnt(" #n ")" ::: "memory")
;     ...
;         for (int t = 0; t < nt; t += 2) {
;             const bool last = (t == nt - 2);
;             const size_t k1 = (size_t)(t + 1) * kstep;
;             const size_t k2 = last ? 0 : (size_t)(t + 2) * kstep, k3 = k2 + kstep;
;             const char* b2 = last ? nB : cB + (size_t)(t + 2) * kstep; const char* b3 = b2 + kstep;
;             PG8_LDB(B0, 0, 0); PG8_LDB(B1, 0, 1); PG8_SCHED; PG8_LDA(At, 0, 0); PG8_STAGE_A(PG8_SA(1, 1), 1, k1, false);
;             PG8_WAIT_V(8); PG8_WAIT_L(0); PG8_BAR; PG8_MMA(0, 0, At, B0); PG8_MMA(0, 1, At, B1); PG8_BAR; PG8_SCHED;
;             PG8_LDA(At, 0, 1); PG8_STAGE(PG8_SB(0, 0), b2, voffB); PG8_STAGE(PG8_SB(0, 1), b2 + hstep, voffB); PG8_STAGE_A(PG8_SA(0, 0), 0, k2, last);
;             PG8_WAIT_V(8); PG8_WAIT_L(0); PG8_BAR; PG8_MMA(1, 0, At, B0); PG8_MMA(1, 1, At, B1); PG8_BAR; PG8_SCHED;
;             PG8_LDB(B0, 1, 0); PG8_LDB(B1, 1, 1); PG8_SCHED; PG8_LDA(At, 1, 0); PG8_STAGE_A(PG8_SA(0, 1), 1, k2, last);
;             PG8_WAIT_V(8); PG8_WAIT_L(0); PG8_BAR; PG8_MMA(0, 0, At, B0); PG8_MMA(0, 1, At, B1); PG8_BAR; PG8_SCHED;
;             PG8_LDA(At, 1, 1); PG8_STAGE(PG8_SB(1, 0), b3, voffB); PG8_STAGE(PG8_SB(1, 1), b3 + hstep, voffB); PG8_STAGE_A(PG8_SA(1, 0), 0, k3, last);
;             PG8_WAIT_V(8); PG8_WAIT_L(0); PG8_BAR; PG8_MMA(1, 0, At, B0); PG8_MMA(1, 1, At, B1); PG8_BAR; PG8_SCHED;
;         }
	s_nop 4
	ds_read_b128 v[0:3], v151
	ds_read_b128 v[4:7], v151 offset:16
	ds_read_b128 v[16:19], v151 offset:2048
	ds_read_b128 v[20:23], v151 offset:2064
	ds_read_b128 v[130:133], v152
	ds_read_b128 v[134:137], v152 offset:16
	ds_read_b128 v[154:157], v152 offset:2048
	ds_read_b128 v[158:161], v152 offset:2064
	ds_read_b128 v[8:11], v148 offset:32768
	ds_read_b128 v[12:15], v148 offset:32784
	ds_read_b128 v[24:27], v148 offset:34816
	ds_read_b128 v[28:31], v148 offset:34832
	ds_read_b128 v[32:35], v148 offset:36864
	ds_read_b128 v[36:39], v148 offset:36880
	ds_read_b128 v[40:43], v148 offset:38912
	ds_read_b128 v[44:47], v148 offset:38928
	s_add_u32 s90, s54, 0x40000
	s_addc_u32 s91, s55, 0
	s_mov_b32 m0, s65
	s_nop 0
	global_load_lds_dwordx4 v142, s[90:91]
	s_nop 0
	s_mov_b32 m0, s66
	s_nop 0
	global_load_lds_dwordx4 v144, s[90:91]
	s_waitcnt vmcnt(8)
	s_waitcnt lgkmcnt(0)
	s_barrier
	s_setprio 1
	v_mfma_scale_f32_16x16x128_f8f6f4 v[124:127], v[0:7], v[8:15], v[124:127], v150, v149 op_sel_hi:[0,0,0]
	v_mfma_scale_f32_16x16x128_f8f6f4 v[120:123], v[16:23], v[8:15], v[120:123], v150, v149 op_sel_hi:[0,0,0]
	v_mfma_scale_f32_16x16x128_f8f6f4 v[108:111], v[0:7], v[24:31], v[108:111], v150, v149 op_sel_hi:[0,0,0]
	v_mfma_scale_f32_16x16x128_f8f6f4 v[104:107], v[16:23], v[24:31], v[104:107], v150, v149 op_sel_hi:[0,0,0]
	v_mfma_scale_f32_16x16x128_f8f6f4 v[92:95], v[0:7], v[32:39], v[138:141], v150, v149 op_sel_hi:[0,0,0]
	v_mfma_scale_f32_16x16x128_f8f6f4 v[88:91], v[16:23], v[32:39], v[210:213], v150, v149 op_sel_hi:[0,0,0]
	v_mfma_scale_f32_16x16x128_f8f6f4 v[76:79], v[0:7], v[40:47], v[214:217], v150, v149 op_sel_hi:[0,0,0]
	v_mfma_scale_f32_16x16x128_f8f6f4 v[72:75], v[16:23], v[40:47], v[218:221], v150, v149 op_sel_hi:[0,0,0]
	v_mfma_scale_f32_16x16x128_f8f6f4 v[116:119], v[130:137], v[8:15], v[116:119], v150, v149 op_sel_hi:[0,0,0]
	v_mfma_scale_f32_16x16x128_f8f6f4 v[112:115], v[154:161], v[8:15], v[112:115], v150, v149 op_sel_hi:[0,0,0]
	v_mfma_scale_f32_16x16x128_f8f6f4 v[100:103], v[130:137], v[24:31], v[100:103], v150, v149 op_sel_hi:[0,0,0]
	v_mfma_scale_f32_16x16x128_f8f6f4 v[96:99], v[154:161], v[24:31], v[96:99], v150, v149 op_sel_hi:[0,0,0]
	v_mfma_scale_f32_16x16x128_f8f6f4 v[84:87], v[130:137], v[32:39], v[178:181], v150, v149 op_sel_hi:[0,0,0]
	v_mfma_scale_f32_16x16x128_f8f6f4 v[80:83], v[154:161], v[32:39], v[182:185], v150, v149 op_sel_hi:[0,0,0]
	v_mfma_scale_f32_16x16x128_f8f6f4 v[68:71], v[130:137], v[40:47], v[186:189], v150, v149 op_sel_hi:[0,0,0]
	v_mfma_scale_f32_16x16x128_f8f6f4 v[64:67], v[154:161], v[40:47], v[190:193], v150, v149 op_sel_hi:[0,0,0]
	s_setprio 0
	s_barrier
	ds_read_b128 v[32:35], v148 offset:49152
	ds_read_b128 v[36:39], v148 offset:49168
	ds_read_b128 v[162:165], v148 offset:51200
	ds_read_b128 v[166:169], v148 offset:51216
	ds_read_b128 v[170:173], v148 offset:53248
	ds_read_b128 v[174:177], v148 offset:53264
	ds_read_b128 v[178:181], v148 offset:55296
	ds_read_b128 v[182:185], v148 offset:55312
	s_add_u32 s90, s42, 0x80
	s_addc_u32 s91, s43, 0
	s_mov_b32 m0, s74
	s_nop 0
	global_load_lds_dwordx4 v143, s[90:91]
	s_add_u32 s42, s42, 0x40080
	s_mov_b32 m0, s75
	s_nop 0
	global_load_lds_dwordx4 v145, s[90:91]
	s_addc_u32 s43, s43, 0
	s_mov_b32 m0, s78
	s_nop 0
	global_load_lds_dwordx4 v143, s[42:43]
	s_nop 0
	s_mov_b32 m0, s79
	s_nop 0
	global_load_lds_dwordx4 v145, s[42:43]
	s_add_u32 s42, s54, 0x80
	s_addc_u32 s43, s55, 0
	s_mov_b32 m0, s76
	s_nop 0
	global_load_lds_dwordx4 v142, s[42:43]
	s_nop 0
	s_mov_b32 m0, s77
	s_nop 0
	global_load_lds_dwordx4 v144, s[42:43]
	s_waitcnt vmcnt(8)
	s_waitcnt lgkmcnt(0)
	s_barrier
	s_setprio 1
	v_mfma_scale_f32_16x16x128_f8f6f4 v[60:63], v[0:7], v[32:39], v[60:63], v150, v149 op_sel_hi:[0,0,0]
	v_mfma_scale_f32_16x16x128_f8f6f4 v[56:59], v[16:23], v[32:39], v[56:59], v150, v149 op_sel_hi:[0,0,0]
	v_mfma_scale_f32_16x16x128_f8f6f4 v[44:47], v[0:7], v[162:169], v[194:197], v150, v149 op_sel_hi:[0,0,0]
	v_mfma_scale_f32_16x16x128_f8f6f4 v[40:43], v[16:23], v[162:169], v[198:201], v150, v149 op_sel_hi:[0,0,0]
	v_mfma_scale_f32_16x16x128_f8f6f4 v[28:31], v[0:7], v[170:177], v[202:205], v150, v149 op_sel_hi:[0,0,0]
	v_mfma_scale_f32_16x16x128_f8f6f4 v[24:27], v[16:23], v[170:177], v[206:209], v150, v149 op_sel_hi:[0,0,0]
	v_mfma_scale_f32_16x16x128_f8f6f4 v[12:15], v[0:7], v[178:185], v[222:225], v150, v149 op_sel_hi:[0,0,0]
	v_mfma_scale_f32_16x16x128_f8f6f4 v[8:11], v[16:23], v[178:185], v[226:229], v150, v149 op_sel_hi:[0,0,0]
	v_mfma_scale_f32_16x16x128_f8f6f4 v[52:55], v[130:137], v[32:39], v[52:55], v150, v149 op_sel_hi:[0,0,0]
	v_mfma_scale_f32_16x16x128_f8f6f4 v[48:51], v[154:161], v[32:39], v[48:51], v150, v149 op_sel_hi:[0,0,0]
	v_mfma_scale_f32_16x16x128_f8f6f4 v[36:39], v[130:137], v[162:169], v[230:233], v150, v149 op_sel_hi:[0,0,0]
	v_mfma_scale_f32_16x16x128_f8f6f4 v[32:35], v[154:161], v[162:169], v[234:237], v150, v149 op_sel_hi:[0,0,0]
	v_mfma_scale_f32_16x16x128_f8f6f4 v[20:23], v[130:137], v[170:177], v[238:241], v150, v149 op_sel_hi:[0,0,0]
	v_mfma_scale_f32_16x16x128_f8f6f4 v[16:19], v[154:161], v[170:177], v[242:245], v150, v149 op_sel_hi:[0,0,0]
	v_mfma_scale_f32_16x16x128_f8f6f4 v[4:7], v[130:137], v[178:185], v[246:249], v150, v149 op_sel_hi:[0,0,0]
	v_mfma_scale_f32_16x16x128_f8f6f4 v[0:3], v[154:161], v[178:185], v[250:253], v150, v149 op_sel_hi:[0,0,0]
	s_setprio 0
	s_barrier
	s_add_i32 s23, s23, 2
	s_add_u32 s40, s40, 0x100
	s_addc_u32 s41, s41, 0
	s_cmp_gt_u32 s23, 13
	s_cbranch_scc0 .LBB4_1541
	s_and_b64 vcc, exec, s[10:11]
	s_cbranch_vccz .LBB4_1544
	s_barrier
